# mix GEMM mid hook: both halves gate-logit loads issued up front (free registers), on top of the fragment-order layout
# speedup vs baseline: 1.0019x; 1.0019x over previous
.Lmid1046:
	ds_read_b128 v[136:139], v175
	ds_read_b128 v[140:143], v175 offset:1024
	ds_read_b128 v[144:147], v175 offset:2048
	ds_read_b128 v[148:151], v175 offset:3072
	ds_read_b128 v[152:155], v176
	ds_read_b128 v[156:159], v176 offset:1024
	ds_read_b128 v[160:163], v176 offset:2048
	ds_read_b128 v[178:181], v176 offset:3072
	ds_read_b128 v[182:185], v174 offset:32768
	ds_read_b128 v[186:189], v174 offset:33792
	ds_read_b128 v[190:193], v174 offset:34816
	ds_read_b128 v[194:197], v174 offset:35840
	ds_read_b128 v[198:201], v174 offset:36864
	ds_read_b128 v[202:205], v174 offset:37888
	ds_read_b128 v[206:209], v174 offset:38912
	ds_read_b128 v[210:213], v174 offset:39936
	s_add_u32 s28, s25, 0x40100
	s_addc_u32 s29, s33, 0
	s_mov_b32 s25, m0
	s_mov_b32 m0, s85
	s_nop 2
	global_load_lds_dwordx4 v165, s[28:29]
	s_mov_b32 m0, s25
	s_nop 0
	s_mov_b32 s25, m0
	s_mov_b32 m0, s86
	s_nop 2
	global_load_lds_dwordx4 v167, s[28:29]
	s_mov_b32 m0, s25
	s_waitcnt vmcnt(8)
	s_waitcnt lgkmcnt(0)
	s_barrier
	s_setprio 1
	s_waitcnt lgkmcnt(7)
	v_mfma_f32_16x16x32_bf16 v[26:29], v[136:139], v[182:185], v[26:29]
	v_mfma_f32_16x16x32_bf16 v[30:33], v[144:147], v[182:185], v[30:33]
	s_waitcnt lgkmcnt(5)
	v_mfma_f32_16x16x32_bf16 v[50:53], v[136:139], v[190:193], v[50:53]
	v_mfma_f32_16x16x32_bf16 v[54:57], v[144:147], v[190:193], v[54:57]
	s_waitcnt lgkmcnt(3)
	v_mfma_f32_16x16x32_bf16 v[74:77], v[136:139], v[198:201], v[74:77]
	v_mfma_f32_16x16x32_bf16 v[78:81], v[144:147], v[198:201], v[78:81]
	s_waitcnt lgkmcnt(1)
	v_mfma_f32_16x16x32_bf16 v[94:97], v[136:139], v[206:209], v[94:97]
	v_mfma_f32_16x16x32_bf16 v[102:105], v[144:147], v[206:209], v[102:105]
	v_mfma_f32_16x16x32_bf16 v[26:29], v[140:143], v[186:189], v[26:29]
	v_mfma_f32_16x16x32_bf16 v[30:33], v[148:151], v[186:189], v[30:33]
	v_mfma_f32_16x16x32_bf16 v[50:53], v[140:143], v[194:197], v[50:53]
	v_mfma_f32_16x16x32_bf16 v[54:57], v[148:151], v[194:197], v[54:57]
	v_mfma_f32_16x16x32_bf16 v[74:77], v[140:143], v[202:205], v[74:77]
	v_mfma_f32_16x16x32_bf16 v[78:81], v[148:151], v[202:205], v[78:81]
	s_waitcnt lgkmcnt(0)
	v_mfma_f32_16x16x32_bf16 v[94:97], v[140:143], v[210:213], v[94:97]
	v_mfma_f32_16x16x32_bf16 v[102:105], v[148:151], v[210:213], v[102:105]
	s_setprio 0
	s_setprio 1
	v_mfma_f32_16x16x32_bf16 v[38:41], v[152:155], v[182:185], v[38:41]
	v_mfma_f32_16x16x32_bf16 v[42:45], v[160:163], v[182:185], v[42:45]
	v_mfma_f32_16x16x32_bf16 v[62:65], v[152:155], v[190:193], v[62:65]
	v_mfma_f32_16x16x32_bf16 v[66:69], v[160:163], v[190:193], v[66:69]
	v_mfma_f32_16x16x32_bf16 v[82:85], v[152:155], v[198:201], v[82:85]
	v_mfma_f32_16x16x32_bf16 v[90:93], v[160:163], v[198:201], v[90:93]
	v_mfma_f32_16x16x32_bf16 v[106:109], v[152:155], v[206:209], v[106:109]
	v_mfma_f32_16x16x32_bf16 v[114:117], v[160:163], v[206:209], v[114:117]
	v_mfma_f32_16x16x32_bf16 v[38:41], v[156:159], v[186:189], v[38:41]
	v_mfma_f32_16x16x32_bf16 v[42:45], v[178:181], v[186:189], v[42:45]
	v_mfma_f32_16x16x32_bf16 v[62:65], v[156:159], v[194:197], v[62:65]
	v_mfma_f32_16x16x32_bf16 v[66:69], v[178:181], v[194:197], v[66:69]
	v_mfma_f32_16x16x32_bf16 v[82:85], v[156:159], v[202:205], v[82:85]
	v_mfma_f32_16x16x32_bf16 v[90:93], v[178:181], v[202:205], v[90:93]
	v_mfma_f32_16x16x32_bf16 v[106:109], v[156:159], v[210:213], v[106:109]
	v_mfma_f32_16x16x32_bf16 v[114:117], v[178:181], v[210:213], v[114:117]
	s_setprio 0
	s_barrier
	ds_read_b128 v[182:185], v174 offset:49152
	ds_read_b128 v[186:189], v174 offset:50176
	ds_read_b128 v[190:193], v174 offset:51200
	ds_read_b128 v[194:197], v174 offset:52224
	ds_read_b128 v[198:201], v174 offset:53248
	ds_read_b128 v[202:205], v174 offset:54272
	ds_read_b128 v[206:209], v174 offset:55296
	ds_read_b128 v[210:213], v174 offset:56320
	s_add_u32 s28, s23, 0x180
	s_addc_u32 s29, s24, 0
	s_mov_b32 s25, m0
	s_mov_b32 m0, s92
	s_nop 2
	global_load_lds_dwordx4 v166, s[28:29]
	s_mov_b32 m0, s25
	s_nop 0
	s_mov_b32 s25, m0
	s_mov_b32 m0, s93
	s_nop 2
	global_load_lds_dwordx4 v168, s[28:29]
	s_mov_b32 m0, s25
	s_add_u32 s28, s23, 0x40180
	s_addc_u32 s29, s24, 0
	s_mov_b32 s23, m0
	s_mov_b32 m0, s96
	s_nop 2
	global_load_lds_dwordx4 v166, s[28:29]
	s_mov_b32 m0, s23
	s_nop 0
	s_mov_b32 s23, m0
	s_mov_b32 m0, s97
	s_nop 2
	global_load_lds_dwordx4 v168, s[28:29]
	s_mov_b32 m0, s23
	s_nop 0
	s_mov_b32 s23, m0
	s_mov_b32 m0, s94
	s_nop 2
	global_load_lds_dwordx4 v165, s[58:59]
	s_mov_b32 m0, s23
	s_nop 0
	s_mov_b32 s23, m0
	s_mov_b32 m0, s95
	s_nop 2
	global_load_lds_dwordx4 v167, s[58:59]
	s_mov_b32 m0, s23
	s_waitcnt vmcnt(8)
	s_waitcnt lgkmcnt(0)
	s_barrier
	s_setprio 1
	s_waitcnt lgkmcnt(7)
	v_mfma_f32_16x16x32_bf16 v[118:121], v[136:139], v[182:185], v[118:121]
	v_mfma_f32_16x16x32_bf16 v[126:129], v[144:147], v[182:185], v[126:129]
	s_waitcnt lgkmcnt(5)
	v_mfma_f32_16x16x32_bf16 v[98:101], v[136:139], v[190:193], v[98:101]
	v_mfma_f32_16x16x32_bf16 v[86:89], v[144:147], v[190:193], v[86:89]
	s_waitcnt lgkmcnt(3)
	v_mfma_f32_16x16x32_bf16 v[46:49], v[136:139], v[198:201], v[46:49]
	v_mfma_f32_16x16x32_bf16 v[34:37], v[144:147], v[198:201], v[34:37]
	s_waitcnt lgkmcnt(1)
	v_mfma_f32_16x16x32_bf16 v[14:17], v[136:139], v[206:209], v[14:17]
	v_mfma_f32_16x16x32_bf16 v[10:13], v[144:147], v[206:209], v[10:13]
	v_mfma_f32_16x16x32_bf16 v[118:121], v[140:143], v[186:189], v[118:121]
	v_mfma_f32_16x16x32_bf16 v[126:129], v[148:151], v[186:189], v[126:129]
	v_mfma_f32_16x16x32_bf16 v[98:101], v[140:143], v[194:197], v[98:101]
	v_mfma_f32_16x16x32_bf16 v[86:89], v[148:151], v[194:197], v[86:89]
	v_mfma_f32_16x16x32_bf16 v[46:49], v[140:143], v[202:205], v[46:49]
	v_mfma_f32_16x16x32_bf16 v[34:37], v[148:151], v[202:205], v[34:37]
	s_waitcnt lgkmcnt(0)
	v_mfma_f32_16x16x32_bf16 v[14:17], v[140:143], v[210:213], v[14:17]
	v_mfma_f32_16x16x32_bf16 v[10:13], v[148:151], v[210:213], v[10:13]
	s_setprio 0
	s_setprio 1
	v_mfma_f32_16x16x32_bf16 v[122:125], v[152:155], v[182:185], v[122:125]
	v_mfma_f32_16x16x32_bf16 v[110:113], v[160:163], v[182:185], v[110:113]
	v_mfma_f32_16x16x32_bf16 v[70:73], v[152:155], v[190:193], v[70:73]
	v_mfma_f32_16x16x32_bf16 v[58:61], v[160:163], v[190:193], v[58:61]
	v_mfma_f32_16x16x32_bf16 v[22:25], v[152:155], v[198:201], v[22:25]
	v_mfma_f32_16x16x32_bf16 v[18:21], v[160:163], v[198:201], v[18:21]
	v_mfma_f32_16x16x32_bf16 v[6:9], v[152:155], v[206:209], v[6:9]
	v_mfma_f32_16x16x32_bf16 v[2:5], v[160:163], v[206:209], v[2:5]
	v_mfma_f32_16x16x32_bf16 v[122:125], v[156:159], v[186:189], v[122:125]
	v_mfma_f32_16x16x32_bf16 v[110:113], v[178:181], v[186:189], v[110:113]
	v_mfma_f32_16x16x32_bf16 v[70:73], v[156:159], v[194:197], v[70:73]
	v_mfma_f32_16x16x32_bf16 v[58:61], v[178:181], v[194:197], v[58:61]
	v_mfma_f32_16x16x32_bf16 v[22:25], v[156:159], v[202:205], v[22:25]
	v_mfma_f32_16x16x32_bf16 v[18:21], v[178:181], v[202:205], v[18:21]
	v_mfma_f32_16x16x32_bf16 v[6:9], v[156:159], v[210:213], v[6:9]
	v_mfma_f32_16x16x32_bf16 v[2:5], v[178:181], v[210:213], v[2:5]
	s_setprio 0
	s_barrier
	s_add_i32 s3, s3, 2
	s_add_u32 s56, s56, 0x100
	s_addc_u32 s57, s57, 0
	s_cmp_gt_u32 s3, 5
	s_cbranch_scc0 .LBB0_1046
	s_ashr_i32 s55, s54, 31
	s_lshl_b64 s[24:25], s[54:55], 19
	s_add_u32 s56, s69, s24
	s_addc_u32 s57, s76, s25
	s_ashr_i32 s23, s22, 31
	s_lshl_b64 s[24:25], s[22:23], 19
	s_add_u32 s58, s77, s24
	s_addc_u32 s59, s78, s25
	s_lshl_b32 s3, s60, 18
	s_lshl_b32 s23, s2, 8
	s_lshl_b32 s32, s2, 16
	s_add_i32 s2, s32, s3
	v_lshrrev_b32_e32 v214, 6, v0
	v_lshlrev_b32_e32 v214, 13, v214
	v_and_b32_e32 v215, 63, v0
	v_lshl_add_u32 v214, v215, 3, v214
	v_add_u32_e32 v134, s2, v214
	global_load_dwordx2 v[162:163], v134, s[14:15]
	global_load_dwordx2 v[178:179], v134, s[16:17]
	v_or_b32_e32 v136, 0x200, v134
	v_add_u32_e32 v137, 0x400, v134
	v_add_u32_e32 v138, 0x600, v134
	v_add_u32_e32 v139, 0x800, v134
	v_add_u32_e32 v140, 0xa00, v134
	v_add_u32_e32 v141, 0xc00, v134
	v_add_u32_e32 v161, 0xe00, v134
	global_load_dwordx2 v[180:181], v136, s[14:15]
	global_load_dwordx2 v[182:183], v136, s[16:17]
	global_load_dwordx2 v[158:159], v137, s[14:15]
	global_load_dwordx2 v[156:157], v137, s[16:17]
	global_load_dwordx2 v[154:155], v138, s[14:15]
	global_load_dwordx2 v[152:153], v138, s[16:17]
	global_load_dwordx2 v[150:151], v139, s[14:15]
	global_load_dwordx2 v[148:149], v139, s[16:17]
	global_load_dwordx2 v[146:147], v140, s[14:15]
	global_load_dwordx2 v[144:145], v140, s[16:17]
	global_load_dwordx2 v[142:143], v141, s[14:15]
	s_nop 0
	global_load_dwordx2 v[140:141], v141, s[16:17]
	s_nop 0
	global_load_dwordx2 v[138:139], v161, s[14:15]
	global_load_dwordx2 v[136:137], v161, s[16:17]
	v_add_u32_e32 v160, 0x1000, v134
	global_load_dwordx2 v[220:221], v160, s[14:15]
	global_load_dwordx2 v[222:223], v160, s[16:17]
	v_add_u32_e32 v219, 0x1200, v134
	v_add_u32_e32 v215, 0x1400, v134
	v_add_u32_e32 v216, 0x1600, v134
	v_add_u32_e32 v217, 0x1800, v134
	global_load_dwordx2 v[224:225], v219, s[14:15]
	global_load_dwordx2 v[226:227], v219, s[16:17]
	global_load_dwordx2 v[228:229], v215, s[14:15]
	global_load_dwordx2 v[230:231], v215, s[16:17]
	global_load_dwordx2 v[232:233], v216, s[14:15]
	global_load_dwordx2 v[234:235], v216, s[16:17]
	global_load_dwordx2 v[236:237], v217, s[14:15]
	global_load_dwordx2 v[238:239], v217, s[16:17]
	v_add_u32_e32 v219, 0x1a00, v134
	v_add_u32_e32 v215, 0x1c00, v134
	v_add_u32_e32 v216, 0x1e00, v134
	global_load_dwordx2 v[240:241], v219, s[14:15]
	global_load_dwordx2 v[242:243], v219, s[16:17]
	global_load_dwordx2 v[244:245], v215, s[14:15]
	global_load_dwordx2 v[246:247], v215, s[16:17]
	global_load_dwordx2 v[248:249], v216, s[14:15]
	global_load_dwordx2 v[250:251], v216, s[16:17]
	s_and_b64 s[2:3], s[4:5], exec
	s_cselect_b32 s2, s57, s65
	s_cselect_b32 s3, s56, s64
	s_cselect_b32 s24, s59, s63
	s_cselect_b32 s25, s58, s62
	s_add_u32 s28, s64, 0x500
	s_addc_u32 s29, s65, 0
	s_add_u32 s30, s62, 0x500
	s_addc_u32 s31, s63, 0
	s_mov_b32 s33, 6
	s_waitcnt vmcnt(31)
	v_cvt_pk_f32_fp8_e32 v[184:185], v162
	s_waitcnt vmcnt(30)
	v_cvt_pk_f32_fp8_e32 v[190:191], v178
	v_cvt_pk_f32_fp8_e32 v[188:189], v163
	v_cvt_pk_f32_fp8_sdwa v[192:193], v178 src0_sel:WORD_1
	v_cvt_pk_f32_fp8_e32 v[194:195], v179
	v_max_f32_e32 v161, v190, v190
	v_max_f32_e32 v190, v191, v191
	v_med3_f32 v161, v161, s35, v177
	v_med3_f32 v184, v184, s35, v177
	v_max_f32_e32 v191, v192, v192
	v_max_f32_e32 v192, v193, v193
	v_max_f32_e32 v193, v194, v194
	v_max_f32_e32 v194, v195, v195
	v_med3_f32 v190, v190, s35, v177
	v_med3_f32 v185, v185, s35, v177
	v_med3_f32 v188, v188, s35, v177
	v_mul_f32_e32 v161, 0xbfb8aa3b, v161
	v_mul_f32_e32 v195, 0xbfb8aa3b, v184
	v_cvt_pk_f32_fp8_sdwa v[186:187], v162 src0_sel:WORD_1
	v_cvt_pk_f32_fp8_sdwa v[162:163], v163 src0_sel:WORD_1
	v_med3_f32 v194, v194, s35, v177
	v_med3_f32 v189, v189, s35, v177
	v_mul_f32_e32 v190, 0xbfb8aa3b, v190
	v_mul_f32_e32 v196, 0xbfb8aa3b, v185
	v_mul_f32_e32 v199, 0xbfb8aa3b, v188
	v_exp_f32_e32 v184, v161
	v_exp_f32_e32 v161, v195
	v_mul_f32_e32 v200, 0xbfb8aa3b, v194
	v_mul_f32_e32 v189, 0xbfb8aa3b, v189
	v_exp_f32_e32 v185, v190
	v_exp_f32_e32 v190, v196
	v_exp_f32_e32 v194, v199
	v_exp_f32_e32 v195, v189
	v_cvt_pk_f32_fp8_sdwa v[178:179], v179 src0_sel:WORD_1
	v_add_f32_e32 v161, 1.0, v161
	v_add_f32_e32 v189, 1.0, v190
	v_rcp_f32_e32 v190, v161
	v_add_f32_e32 v161, 1.0, v194
	v_med3_f32 v162, v162, s35, v177
	v_rcp_f32_e32 v194, v161
	v_add_f32_e32 v161, 1.0, v195
	v_mul_f32_e32 v162, 0xbfb8aa3b, v162
	v_rcp_f32_e32 v195, v161
	v_max_f32_e32 v161, v178, v178
	v_exp_f32_e32 v178, v162
	v_med3_f32 v161, v161, s35, v177
	v_med3_f32 v163, v163, s35, v177
	v_mul_f32_e32 v161, 0xbfb8aa3b, v161
	v_mul_f32_e32 v163, 0xbfb8aa3b, v163
	v_exp_f32_e32 v162, v161
	v_add_f32_e32 v161, 1.0, v178
	v_max_f32_e32 v178, v179, v179
	v_exp_f32_e32 v179, v163
	v_med3_f32 v191, v191, s35, v177
	v_med3_f32 v186, v186, s35, v177
	v_med3_f32 v192, v192, s35, v177
	v_med3_f32 v187, v187, s35, v177
	v_mul_f32_e32 v191, 0xbfb8aa3b, v191
	v_mul_f32_e32 v197, 0xbfb8aa3b, v186
	v_mul_f32_e32 v192, 0xbfb8aa3b, v192
	v_mul_f32_e32 v198, 0xbfb8aa3b, v187
	v_med3_f32 v178, v178, s35, v177
	v_exp_f32_e32 v186, v191
	v_exp_f32_e32 v191, v197
	v_exp_f32_e32 v187, v192
	v_exp_f32_e32 v192, v198
	v_mul_f32_e32 v163, 0xbfb8aa3b, v178
	v_exp_f32_e32 v163, v163
	v_rcp_f32_e32 v178, v161
	v_add_f32_e32 v161, 1.0, v179
	v_med3_f32 v193, v193, s35, v177
	v_rcp_f32_e32 v179, v161
	v_mul_f32_e32 v193, 0xbfb8aa3b, v193
	v_exp_f32_e32 v188, v193
	v_add_f32_e32 v193, 1.0, v191
	v_add_f32_e32 v196, 1.0, v192
	v_rcp_f32_e32 v192, v193
	v_rcp_f32_e32 v193, v196
	v_pk_add_f32 v[162:163], v[162:163], 1.0 op_sel_hi:[1,0]
	v_pk_add_f32 v[186:187], v[186:187], 1.0 op_sel_hi:[1,0]
	v_pk_mul_f32 v[162:163], v[178:179], v[162:163]
	v_pk_mul_f32 v[186:187], v[192:193], v[186:187]
	v_pk_mul_f32 v[32:33], v[32:33], v[162:163]
	s_waitcnt vmcnt(29)
	v_cvt_pk_f32_fp8_e32 v[162:163], v180
	v_pk_mul_f32 v[28:29], v[28:29], v[186:187]
	s_waitcnt vmcnt(28)
	v_cvt_pk_f32_fp8_e32 v[186:187], v182
	v_rcp_f32_e32 v191, v189
	v_med3_f32 v162, v162, s35, v177
	v_mul_f32_e32 v162, 0xbfb8aa3b, v162
	v_max_f32_e32 v161, v186, v186
	v_exp_f32_e32 v186, v162
	v_exp_f32_e32 v189, v200
	v_med3_f32 v161, v161, s35, v177
	v_cvt_pk_f32_fp8_sdwa v[178:179], v180 src0_sel:WORD_1
	v_mul_f32_e32 v161, 0xbfb8aa3b, v161
	v_med3_f32 v163, v163, s35, v177
	v_pk_add_f32 v[184:185], v[184:185], 1.0 op_sel_hi:[1,0]
	v_exp_f32_e32 v162, v161
	v_add_f32_e32 v161, 1.0, v186
	v_mul_f32_e32 v163, 0xbfb8aa3b, v163
	v_pk_mul_f32 v[184:185], v[190:191], v[184:185]
	v_rcp_f32_e32 v186, v161
	v_max_f32_e32 v161, v187, v187
	v_exp_f32_e32 v187, v163
	v_pk_mul_f32 v[26:27], v[26:27], v[184:185]
	v_pk_add_f32 v[184:185], v[188:189], 1.0 op_sel_hi:[1,0]
	v_cvt_pk_f32_fp8_sdwa v[188:189], v182 src0_sel:WORD_1
	v_med3_f32 v161, v161, s35, v177
	v_mul_f32_e32 v161, 0xbfb8aa3b, v161
	v_med3_f32 v178, v178, s35, v177
	v_exp_f32_e32 v163, v161
	v_add_f32_e32 v161, 1.0, v187
	v_mul_f32_e32 v178, 0xbfb8aa3b, v178
	v_pk_mul_f32 v[184:185], v[194:195], v[184:185]
	v_rcp_f32_e32 v187, v161
	v_max_f32_e32 v161, v188, v188
	v_exp_f32_e32 v188, v178
	v_pk_mul_f32 v[30:31], v[30:31], v[184:185]
	v_cvt_pk_f32_fp8_e32 v[184:185], v181
	v_med3_f32 v161, v161, s35, v177
	v_med3_f32 v179, v179, s35, v177
	v_mul_f32_e32 v161, 0xbfb8aa3b, v161
	v_mul_f32_e32 v179, 0xbfb8aa3b, v179
	v_pk_add_f32 v[162:163], v[162:163], 1.0 op_sel_hi:[1,0]
	v_exp_f32_e32 v178, v161
	v_add_f32_e32 v161, 1.0, v188
	v_max_f32_e32 v188, v189, v189
	v_exp_f32_e32 v189, v179
	v_pk_mul_f32 v[162:163], v[186:187], v[162:163]
	v_cvt_pk_f32_fp8_e32 v[190:191], v183
	v_pk_mul_f32 v[38:39], v[38:39], v[162:163]
	v_med3_f32 v162, v184, s35, v177
	v_med3_f32 v188, v188, s35, v177
	v_mul_f32_e32 v162, 0xbfb8aa3b, v162
	v_mul_f32_e32 v179, 0xbfb8aa3b, v188
	v_rcp_f32_e32 v188, v161
	v_add_f32_e32 v161, 1.0, v189
	v_exp_f32_e32 v163, v162
	v_exp_f32_e32 v179, v179
	v_rcp_f32_e32 v189, v161
	v_med3_f32 v161, v190, s35, v177
	v_mul_f32_e32 v161, 0xbfb8aa3b, v161
	v_exp_f32_e32 v162, v161
	v_add_f32_e32 v161, 1.0, v163
	v_cvt_pk_f32_fp8_sdwa v[180:181], v181 src0_sel:WORD_1
	v_pk_add_f32 v[178:179], v[178:179], 1.0 op_sel_hi:[1,0]
	v_med3_f32 v163, v185, s35, v177
	v_pk_mul_f32 v[178:179], v[188:189], v[178:179]
	v_mul_f32_e32 v163, 0xbfb8aa3b, v163
	v_pk_mul_f32 v[40:41], v[40:41], v[178:179]
	v_exp_f32_e32 v179, v163
	v_cvt_pk_f32_fp8_sdwa v[182:183], v183 src0_sel:WORD_1
	v_rcp_f32_e32 v178, v161
	v_med3_f32 v161, v191, s35, v177
	v_mul_f32_e32 v161, 0xbfb8aa3b, v161
	v_med3_f32 v180, v180, s35, v177
	v_exp_f32_e32 v163, v161
	v_add_f32_e32 v161, 1.0, v179
	v_mul_f32_e32 v180, 0xbfb8aa3b, v180
	v_rcp_f32_e32 v179, v161
	v_max_f32_e32 v161, v182, v182
	v_exp_f32_e32 v182, v180
	v_med3_f32 v161, v161, s35, v177
	v_med3_f32 v181, v181, s35, v177
	v_mul_f32_e32 v161, 0xbfb8aa3b, v161
	v_mul_f32_e32 v181, 0xbfb8aa3b, v181
	v_exp_f32_e32 v180, v161
	v_add_f32_e32 v161, 1.0, v182
	v_max_f32_e32 v182, v183, v183
	v_exp_f32_e32 v183, v181
	v_med3_f32 v182, v182, s35, v177
	v_mul_f32_e32 v181, 0xbfb8aa3b, v182
	v_exp_f32_e32 v181, v181
	v_rcp_f32_e32 v182, v161
	v_add_f32_e32 v161, 1.0, v183
	v_pk_add_f32 v[162:163], v[162:163], 1.0 op_sel_hi:[1,0]
	v_rcp_f32_e32 v183, v161
	v_pk_mul_f32 v[162:163], v[178:179], v[162:163]
	v_pk_add_f32 v[180:181], v[180:181], 1.0 op_sel_hi:[1,0]
	v_pk_mul_f32 v[42:43], v[42:43], v[162:163]
	s_waitcnt vmcnt(27)
	v_cvt_pk_f32_fp8_e32 v[162:163], v158
	v_pk_mul_f32 v[178:179], v[182:183], v[180:181]
	s_waitcnt vmcnt(26)
	v_cvt_pk_f32_fp8_e32 v[182:183], v156
	v_pk_mul_f32 v[44:45], v[44:45], v[178:179]
	v_med3_f32 v162, v162, s35, v177
	v_mul_f32_e32 v162, 0xbfb8aa3b, v162
	v_max_f32_e32 v161, v182, v182
	v_exp_f32_e32 v182, v162
	v_med3_f32 v161, v161, s35, v177
	v_cvt_pk_f32_fp8_sdwa v[178:179], v158 src0_sel:WORD_1
	v_mul_f32_e32 v161, 0xbfb8aa3b, v161
	v_med3_f32 v163, v163, s35, v177
	v_exp_f32_e32 v162, v161
	v_add_f32_e32 v161, 1.0, v182
	v_mul_f32_e32 v163, 0xbfb8aa3b, v163
	v_rcp_f32_e32 v182, v161
	v_max_f32_e32 v161, v183, v183
	v_exp_f32_e32 v183, v163
	v_cvt_pk_f32_fp8_sdwa v[184:185], v156 src0_sel:WORD_1
	v_med3_f32 v161, v161, s35, v177
	v_mul_f32_e32 v161, 0xbfb8aa3b, v161
	v_med3_f32 v178, v178, s35, v177
	v_exp_f32_e32 v163, v161
	v_add_f32_e32 v161, 1.0, v183
	v_mul_f32_e32 v178, 0xbfb8aa3b, v178
	v_rcp_f32_e32 v183, v161
	v_max_f32_e32 v161, v184, v184
	v_exp_f32_e32 v184, v178
	v_cvt_pk_f32_fp8_e32 v[180:181], v159
	v_med3_f32 v161, v161, s35, v177
	v_med3_f32 v179, v179, s35, v177
	v_mul_f32_e32 v161, 0xbfb8aa3b, v161
	v_mul_f32_e32 v179, 0xbfb8aa3b, v179
	v_pk_add_f32 v[162:163], v[162:163], 1.0 op_sel_hi:[1,0]
	v_cvt_pk_f32_fp8_sdwa v[158:159], v159 src0_sel:WORD_1
	v_exp_f32_e32 v178, v161
	v_add_f32_e32 v161, 1.0, v184
	v_max_f32_e32 v184, v185, v185
	v_exp_f32_e32 v185, v179
	v_pk_mul_f32 v[162:163], v[182:183], v[162:163]
	v_cvt_pk_f32_fp8_e32 v[186:187], v157
	v_pk_mul_f32 v[50:51], v[50:51], v[162:163]
	v_med3_f32 v162, v180, s35, v177
	v_med3_f32 v184, v184, s35, v177
	v_mul_f32_e32 v162, 0xbfb8aa3b, v162
	v_cvt_pk_f32_fp8_sdwa v[156:157], v157 src0_sel:WORD_1
	v_mul_f32_e32 v179, 0xbfb8aa3b, v184
	v_rcp_f32_e32 v184, v161
	v_add_f32_e32 v161, 1.0, v185
	v_exp_f32_e32 v163, v162
	v_exp_f32_e32 v179, v179
	v_rcp_f32_e32 v185, v161
	v_med3_f32 v158, v158, s35, v177
	v_med3_f32 v159, v159, s35, v177
	v_med3_f32 v161, v186, s35, v177
	v_mul_f32_e32 v158, 0xbfb8aa3b, v158
	v_mul_f32_e32 v159, 0xbfb8aa3b, v159
	v_mul_f32_e32 v161, 0xbfb8aa3b, v161
	v_exp_f32_e32 v158, v158
	v_exp_f32_e32 v159, v159
	v_exp_f32_e32 v162, v161
	v_add_f32_e32 v161, 1.0, v163
	v_pk_add_f32 v[178:179], v[178:179], 1.0 op_sel_hi:[1,0]
	v_med3_f32 v163, v181, s35, v177
	v_med3_f32 v156, v156, s35, v177
	v_med3_f32 v157, v157, s35, v177
	v_pk_mul_f32 v[178:179], v[184:185], v[178:179]
	v_mul_f32_e32 v163, 0xbfb8aa3b, v163
	v_mul_f32_e32 v156, 0xbfb8aa3b, v156
	v_mul_f32_e32 v157, 0xbfb8aa3b, v157
	v_pk_mul_f32 v[52:53], v[52:53], v[178:179]
	v_exp_f32_e32 v179, v163
	v_exp_f32_e32 v156, v156
	v_add_f32_e32 v158, 1.0, v158
	v_exp_f32_e32 v157, v157
	v_add_f32_e32 v159, 1.0, v159
	v_rcp_f32_e32 v178, v161
	v_rcp_f32_e32 v158, v158
	v_rcp_f32_e32 v159, v159
	v_med3_f32 v161, v187, s35, v177
	v_mul_f32_e32 v161, 0xbfb8aa3b, v161
	v_exp_f32_e32 v163, v161
	v_add_f32_e32 v161, 1.0, v179
	v_pk_add_f32 v[156:157], v[156:157], 1.0 op_sel_hi:[1,0]
	v_rcp_f32_e32 v179, v161
	v_pk_mul_f32 v[156:157], v[158:159], v[156:157]
	v_pk_add_f32 v[162:163], v[162:163], 1.0 op_sel_hi:[1,0]
	v_pk_mul_f32 v[56:57], v[56:57], v[156:157]
	s_waitcnt vmcnt(25)
	v_cvt_pk_f32_fp8_e32 v[156:157], v154
	v_pk_mul_f32 v[162:163], v[178:179], v[162:163]
	s_waitcnt vmcnt(24)
	v_cvt_pk_f32_fp8_e32 v[178:179], v152
	v_cvt_pk_f32_fp8_sdwa v[158:159], v154 src0_sel:WORD_1
	v_med3_f32 v156, v156, s35, v177
	v_mul_f32_e32 v156, 0xbfb8aa3b, v156
	v_max_f32_e32 v161, v178, v178
	v_exp_f32_e32 v178, v156
	v_med3_f32 v157, v157, s35, v177
	v_med3_f32 v156, v161, s35, v177
	v_add_f32_e32 v161, 1.0, v178
	v_mul_f32_e32 v157, 0xbfb8aa3b, v157
	v_rcp_f32_e32 v178, v161
	v_max_f32_e32 v161, v179, v179
	v_exp_f32_e32 v179, v157
	v_cvt_pk_f32_fp8_sdwa v[180:181], v152 src0_sel:WORD_1
	v_med3_f32 v158, v158, s35, v177
	v_med3_f32 v157, v161, s35, v177
	v_add_f32_e32 v161, 1.0, v179
	v_mul_f32_e32 v158, 0xbfb8aa3b, v158
	v_rcp_f32_e32 v179, v161
	v_max_f32_e32 v161, v180, v180
	v_exp_f32_e32 v180, v158
	v_med3_f32 v159, v159, s35, v177
	v_pk_mul_f32 v[54:55], v[54:55], v[162:163]
	v_cvt_pk_f32_fp8_e32 v[162:163], v155
	v_cvt_pk_f32_fp8_sdwa v[154:155], v155 src0_sel:WORD_1
	v_mul_f32_e32 v156, 0xbfb8aa3b, v156
	v_mul_f32_e32 v157, 0xbfb8aa3b, v157
	v_mul_f32_e32 v159, 0xbfb8aa3b, v159
	v_exp_f32_e32 v156, v156
	v_exp_f32_e32 v157, v157
	v_med3_f32 v158, v161, s35, v177
	v_add_f32_e32 v161, 1.0, v180
	v_max_f32_e32 v180, v181, v181
	v_exp_f32_e32 v181, v159
	v_med3_f32 v180, v180, s35, v177
	v_cvt_pk_f32_fp8_e32 v[182:183], v153
	v_cvt_pk_f32_fp8_sdwa v[152:153], v153 src0_sel:WORD_1
	v_mul_f32_e32 v158, 0xbfb8aa3b, v158
	v_mul_f32_e32 v159, 0xbfb8aa3b, v180
	v_exp_f32_e32 v158, v158
	v_exp_f32_e32 v159, v159
	v_rcp_f32_e32 v180, v161
	v_add_f32_e32 v161, 1.0, v181
	v_pk_add_f32 v[156:157], v[156:157], 1.0 op_sel_hi:[1,0]
	v_med3_f32 v154, v154, s35, v177
	v_med3_f32 v155, v155, s35, v177
	v_rcp_f32_e32 v181, v161
	v_pk_mul_f32 v[156:157], v[178:179], v[156:157]
	v_mul_f32_e32 v154, 0xbfb8aa3b, v154
	v_mul_f32_e32 v155, 0xbfb8aa3b, v155
	v_pk_mul_f32 v[62:63], v[62:63], v[156:157]
	v_exp_f32_e32 v154, v154
	v_exp_f32_e32 v155, v155
	v_med3_f32 v157, v162, s35, v177
	v_pk_add_f32 v[158:159], v[158:159], 1.0 op_sel_hi:[1,0]
	v_mul_f32_e32 v157, 0xbfb8aa3b, v157
	v_med3_f32 v152, v152, s35, v177
	v_med3_f32 v153, v153, s35, v177
	v_pk_mul_f32 v[158:159], v[180:181], v[158:159]
	v_exp_f32_e32 v157, v157
	v_mul_f32_e32 v152, 0xbfb8aa3b, v152
	v_mul_f32_e32 v153, 0xbfb8aa3b, v153
	v_pk_mul_f32 v[64:65], v[64:65], v[158:159]
	v_exp_f32_e32 v152, v152
	v_add_f32_e32 v154, 1.0, v154
	v_exp_f32_e32 v153, v153
	v_add_f32_e32 v155, 1.0, v155
	v_med3_f32 v159, v163, s35, v177
	v_rcp_f32_e32 v154, v154
	v_rcp_f32_e32 v155, v155
	v_mul_f32_e32 v159, 0xbfb8aa3b, v159
	v_add_f32_e32 v157, 1.0, v157
	v_exp_f32_e32 v159, v159
	v_rcp_f32_e32 v158, v157
	v_pk_add_f32 v[152:153], v[152:153], 1.0 op_sel_hi:[1,0]
	v_med3_f32 v156, v182, s35, v177
	v_med3_f32 v157, v183, s35, v177
	v_pk_mul_f32 v[152:153], v[154:155], v[152:153]
	v_mul_f32_e32 v156, 0xbfb8aa3b, v156
	v_mul_f32_e32 v157, 0xbfb8aa3b, v157
	v_pk_mul_f32 v[68:69], v[68:69], v[152:153]
	s_waitcnt vmcnt(23)
	v_cvt_pk_f32_fp8_e32 v[152:153], v150
	v_exp_f32_e32 v156, v156
	v_exp_f32_e32 v157, v157
	v_add_f32_e32 v159, 1.0, v159
	v_rcp_f32_e32 v159, v159
	v_pk_add_f32 v[156:157], v[156:157], 1.0 op_sel_hi:[1,0]
	v_med3_f32 v152, v152, s35, v177
	v_pk_mul_f32 v[156:157], v[158:159], v[156:157]
	s_waitcnt vmcnt(22)
	v_cvt_pk_f32_fp8_e32 v[158:159], v148
	v_mul_f32_e32 v152, 0xbfb8aa3b, v152
	v_exp_f32_e32 v161, v152
	v_cvt_pk_f32_fp8_sdwa v[154:155], v150 src0_sel:WORD_1
	v_med3_f32 v153, v153, s35, v177
	v_mul_f32_e32 v153, 0xbfb8aa3b, v153
	v_cvt_pk_f32_fp8_sdwa v[162:163], v148 src0_sel:WORD_1
	v_med3_f32 v152, v158, s35, v177
	v_add_f32_e32 v158, 1.0, v161
	v_exp_f32_e32 v161, v153
	v_med3_f32 v154, v154, s35, v177
	v_mul_f32_e32 v154, 0xbfb8aa3b, v154
	v_med3_f32 v153, v159, s35, v177
	v_add_f32_e32 v159, 1.0, v161
	v_max_f32_e32 v161, v162, v162
	v_exp_f32_e32 v162, v154
	v_med3_f32 v155, v155, s35, v177
	v_pk_mul_f32 v[66:67], v[66:67], v[156:157]
	v_cvt_pk_f32_fp8_e32 v[156:157], v151
	v_cvt_pk_f32_fp8_sdwa v[150:151], v151 src0_sel:WORD_1
	v_mul_f32_e32 v152, 0xbfb8aa3b, v152
	v_mul_f32_e32 v153, 0xbfb8aa3b, v153
	v_mul_f32_e32 v155, 0xbfb8aa3b, v155
	v_exp_f32_e32 v152, v152
	v_exp_f32_e32 v153, v153
	v_med3_f32 v154, v161, s35, v177
	v_add_f32_e32 v161, 1.0, v162
	v_max_f32_e32 v162, v163, v163
	v_exp_f32_e32 v163, v155
	v_rcp_f32_e32 v158, v158
	v_rcp_f32_e32 v159, v159
	v_med3_f32 v162, v162, s35, v177
	v_cvt_pk_f32_fp8_e32 v[178:179], v149
	v_cvt_pk_f32_fp8_sdwa v[148:149], v149 src0_sel:WORD_1
	v_mul_f32_e32 v154, 0xbfb8aa3b, v154
	v_mul_f32_e32 v155, 0xbfb8aa3b, v162
	v_exp_f32_e32 v154, v154
	v_exp_f32_e32 v155, v155
	v_rcp_f32_e32 v162, v161
	v_add_f32_e32 v161, 1.0, v163
	v_pk_add_f32 v[152:153], v[152:153], 1.0 op_sel_hi:[1,0]
	v_med3_f32 v150, v150, s35, v177
	v_med3_f32 v151, v151, s35, v177
	v_rcp_f32_e32 v163, v161
	v_pk_mul_f32 v[152:153], v[158:159], v[152:153]
	v_mul_f32_e32 v150, 0xbfb8aa3b, v150
	v_mul_f32_e32 v151, 0xbfb8aa3b, v151
	v_pk_mul_f32 v[74:75], v[74:75], v[152:153]
	v_exp_f32_e32 v150, v150
	v_exp_f32_e32 v151, v151
	v_med3_f32 v153, v156, s35, v177
	v_pk_add_f32 v[154:155], v[154:155], 1.0 op_sel_hi:[1,0]
	v_mul_f32_e32 v153, 0xbfb8aa3b, v153
	v_med3_f32 v148, v148, s35, v177
	v_med3_f32 v149, v149, s35, v177
	v_pk_mul_f32 v[154:155], v[162:163], v[154:155]
	v_exp_f32_e32 v153, v153
	v_mul_f32_e32 v148, 0xbfb8aa3b, v148
	v_mul_f32_e32 v149, 0xbfb8aa3b, v149
	v_pk_mul_f32 v[76:77], v[76:77], v[154:155]
	v_exp_f32_e32 v148, v148
	v_add_f32_e32 v150, 1.0, v150
	v_exp_f32_e32 v149, v149
	v_add_f32_e32 v151, 1.0, v151
	v_med3_f32 v155, v157, s35, v177
	v_rcp_f32_e32 v150, v150
	v_rcp_f32_e32 v151, v151
	v_mul_f32_e32 v155, 0xbfb8aa3b, v155
	v_add_f32_e32 v153, 1.0, v153
	v_exp_f32_e32 v155, v155
	v_rcp_f32_e32 v154, v153
	v_pk_add_f32 v[148:149], v[148:149], 1.0 op_sel_hi:[1,0]
	v_med3_f32 v152, v178, s35, v177
	v_med3_f32 v153, v179, s35, v177
	v_pk_mul_f32 v[148:149], v[150:151], v[148:149]
	v_mul_f32_e32 v152, 0xbfb8aa3b, v152
	v_mul_f32_e32 v153, 0xbfb8aa3b, v153
	v_pk_mul_f32 v[80:81], v[80:81], v[148:149]
	s_waitcnt vmcnt(21)
	v_cvt_pk_f32_fp8_e32 v[148:149], v146
	v_exp_f32_e32 v152, v152
	v_exp_f32_e32 v153, v153
	v_add_f32_e32 v155, 1.0, v155
	v_rcp_f32_e32 v155, v155
	v_pk_add_f32 v[152:153], v[152:153], 1.0 op_sel_hi:[1,0]
	v_med3_f32 v148, v148, s35, v177
	v_pk_mul_f32 v[152:153], v[154:155], v[152:153]
	s_waitcnt vmcnt(20)
	v_cvt_pk_f32_fp8_e32 v[154:155], v144
	v_mul_f32_e32 v148, 0xbfb8aa3b, v148
	v_exp_f32_e32 v161, v148
	v_cvt_pk_f32_fp8_sdwa v[150:151], v146 src0_sel:WORD_1
	v_med3_f32 v149, v149, s35, v177
	v_mul_f32_e32 v149, 0xbfb8aa3b, v149
	v_med3_f32 v148, v154, s35, v177
	v_add_f32_e32 v154, 1.0, v161
	v_exp_f32_e32 v161, v149
	v_med3_f32 v150, v150, s35, v177
	v_cvt_pk_f32_fp8_sdwa v[156:157], v144 src0_sel:WORD_1
	v_mul_f32_e32 v150, 0xbfb8aa3b, v150
	v_med3_f32 v149, v155, s35, v177
	v_add_f32_e32 v155, 1.0, v161
	v_exp_f32_e32 v161, v150
	v_med3_f32 v151, v151, s35, v177
	v_pk_mul_f32 v[78:79], v[78:79], v[152:153]
	v_cvt_pk_f32_fp8_e32 v[152:153], v147
	v_cvt_pk_f32_fp8_sdwa v[146:147], v147 src0_sel:WORD_1
	v_mul_f32_e32 v148, 0xbfb8aa3b, v148
	v_mul_f32_e32 v149, 0xbfb8aa3b, v149
	v_mul_f32_e32 v151, 0xbfb8aa3b, v151
	v_exp_f32_e32 v148, v148
	v_exp_f32_e32 v149, v149
	v_med3_f32 v150, v156, s35, v177
	v_add_f32_e32 v156, 1.0, v161
	v_exp_f32_e32 v161, v151
	v_rcp_f32_e32 v154, v154
	v_rcp_f32_e32 v155, v155
	v_med3_f32 v157, v157, s35, v177
	v_cvt_pk_f32_fp8_e32 v[158:159], v145
	v_cvt_pk_f32_fp8_sdwa v[144:145], v145 src0_sel:WORD_1
	v_mul_f32_e32 v150, 0xbfb8aa3b, v150
	v_mul_f32_e32 v151, 0xbfb8aa3b, v157
	v_exp_f32_e32 v150, v150
	v_exp_f32_e32 v151, v151
	v_add_f32_e32 v157, 1.0, v161
	v_pk_add_f32 v[148:149], v[148:149], 1.0 op_sel_hi:[1,0]
	v_med3_f32 v146, v146, s35, v177
	v_med3_f32 v147, v147, s35, v177
	v_rcp_f32_e32 v156, v156
	v_rcp_f32_e32 v157, v157
	v_pk_mul_f32 v[148:149], v[154:155], v[148:149]
	v_mul_f32_e32 v146, 0xbfb8aa3b, v146
	v_mul_f32_e32 v147, 0xbfb8aa3b, v147
	v_pk_mul_f32 v[82:83], v[82:83], v[148:149]
	v_exp_f32_e32 v146, v146
	v_exp_f32_e32 v147, v147
	v_med3_f32 v149, v152, s35, v177
	v_pk_add_f32 v[150:151], v[150:151], 1.0 op_sel_hi:[1,0]
	v_mul_f32_e32 v149, 0xbfb8aa3b, v149
	v_med3_f32 v144, v144, s35, v177
	v_med3_f32 v145, v145, s35, v177
	v_pk_mul_f32 v[150:151], v[156:157], v[150:151]
	v_exp_f32_e32 v149, v149
	v_mul_f32_e32 v144, 0xbfb8aa3b, v144
	v_mul_f32_e32 v145, 0xbfb8aa3b, v145
	v_pk_mul_f32 v[84:85], v[84:85], v[150:151]
	v_exp_f32_e32 v144, v144
	v_add_f32_e32 v146, 1.0, v146
	v_exp_f32_e32 v145, v145
	v_add_f32_e32 v147, 1.0, v147
	v_med3_f32 v151, v153, s35, v177
	v_rcp_f32_e32 v146, v146
	v_rcp_f32_e32 v147, v147
	v_mul_f32_e32 v151, 0xbfb8aa3b, v151
	v_add_f32_e32 v149, 1.0, v149
	v_exp_f32_e32 v151, v151
	v_rcp_f32_e32 v150, v149
	v_pk_add_f32 v[144:145], v[144:145], 1.0 op_sel_hi:[1,0]
	v_med3_f32 v148, v158, s35, v177
	v_med3_f32 v149, v159, s35, v177
	v_pk_mul_f32 v[144:145], v[146:147], v[144:145]
	v_mul_f32_e32 v148, 0xbfb8aa3b, v148
	v_mul_f32_e32 v149, 0xbfb8aa3b, v149
	v_pk_mul_f32 v[92:93], v[92:93], v[144:145]
	s_waitcnt vmcnt(19)
	v_cvt_pk_f32_fp8_e32 v[144:145], v142
	v_exp_f32_e32 v148, v148
	v_exp_f32_e32 v149, v149
	v_add_f32_e32 v151, 1.0, v151
	v_rcp_f32_e32 v151, v151
	v_pk_add_f32 v[148:149], v[148:149], 1.0 op_sel_hi:[1,0]
	v_med3_f32 v144, v144, s35, v177
	v_pk_mul_f32 v[148:149], v[150:151], v[148:149]
	s_waitcnt vmcnt(18)
	v_cvt_pk_f32_fp8_e32 v[150:151], v140
	v_mul_f32_e32 v144, 0xbfb8aa3b, v144
	v_exp_f32_e32 v156, v144
	v_cvt_pk_f32_fp8_sdwa v[146:147], v142 src0_sel:WORD_1
	v_med3_f32 v145, v145, s35, v177
	v_mul_f32_e32 v145, 0xbfb8aa3b, v145
	v_med3_f32 v144, v150, s35, v177
	v_add_f32_e32 v150, 1.0, v156
	v_exp_f32_e32 v156, v145
	v_med3_f32 v146, v146, s35, v177
	v_cvt_pk_f32_fp8_sdwa v[152:153], v140 src0_sel:WORD_1
	v_mul_f32_e32 v146, 0xbfb8aa3b, v146
	v_med3_f32 v145, v151, s35, v177
	v_add_f32_e32 v151, 1.0, v156
	v_exp_f32_e32 v156, v146
	v_med3_f32 v147, v147, s35, v177
	v_pk_mul_f32 v[90:91], v[90:91], v[148:149]
	v_cvt_pk_f32_fp8_e32 v[148:149], v143
	v_cvt_pk_f32_fp8_sdwa v[142:143], v143 src0_sel:WORD_1
	v_mul_f32_e32 v144, 0xbfb8aa3b, v144
	v_mul_f32_e32 v145, 0xbfb8aa3b, v145
	v_mul_f32_e32 v147, 0xbfb8aa3b, v147
	v_exp_f32_e32 v144, v144
	v_exp_f32_e32 v145, v145
	v_med3_f32 v146, v152, s35, v177
	v_add_f32_e32 v152, 1.0, v156
	v_exp_f32_e32 v156, v147
	v_rcp_f32_e32 v150, v150
	v_rcp_f32_e32 v151, v151
	v_med3_f32 v153, v153, s35, v177
	v_cvt_pk_f32_fp8_e32 v[154:155], v141
	v_cvt_pk_f32_fp8_sdwa v[140:141], v141 src0_sel:WORD_1
	v_mul_f32_e32 v146, 0xbfb8aa3b, v146
	v_mul_f32_e32 v147, 0xbfb8aa3b, v153
	v_exp_f32_e32 v146, v146
	v_exp_f32_e32 v147, v147
	v_add_f32_e32 v153, 1.0, v156
	v_pk_add_f32 v[144:145], v[144:145], 1.0 op_sel_hi:[1,0]
	v_med3_f32 v142, v142, s35, v177
	v_med3_f32 v143, v143, s35, v177
	v_rcp_f32_e32 v152, v152
	v_rcp_f32_e32 v153, v153
	v_pk_mul_f32 v[144:145], v[150:151], v[144:145]
	v_mul_f32_e32 v142, 0xbfb8aa3b, v142
	v_mul_f32_e32 v143, 0xbfb8aa3b, v143
	v_pk_mul_f32 v[94:95], v[94:95], v[144:145]
	v_exp_f32_e32 v142, v142
	v_exp_f32_e32 v143, v143
	v_med3_f32 v145, v148, s35, v177
	v_pk_add_f32 v[146:147], v[146:147], 1.0 op_sel_hi:[1,0]
	v_mul_f32_e32 v145, 0xbfb8aa3b, v145
	v_med3_f32 v140, v140, s35, v177
	v_med3_f32 v141, v141, s35, v177
	v_pk_mul_f32 v[146:147], v[152:153], v[146:147]
	v_exp_f32_e32 v145, v145
	v_mul_f32_e32 v140, 0xbfb8aa3b, v140
	v_mul_f32_e32 v141, 0xbfb8aa3b, v141
	v_pk_mul_f32 v[96:97], v[96:97], v[146:147]
	v_exp_f32_e32 v140, v140
	v_add_f32_e32 v142, 1.0, v142
	v_exp_f32_e32 v141, v141
	v_add_f32_e32 v143, 1.0, v143
	v_med3_f32 v147, v149, s35, v177
	v_rcp_f32_e32 v142, v142
	v_rcp_f32_e32 v143, v143
	v_mul_f32_e32 v147, 0xbfb8aa3b, v147
	v_add_f32_e32 v145, 1.0, v145
	v_exp_f32_e32 v147, v147
	v_rcp_f32_e32 v146, v145
	v_pk_add_f32 v[140:141], v[140:141], 1.0 op_sel_hi:[1,0]
	v_med3_f32 v144, v154, s35, v177
	v_med3_f32 v145, v155, s35, v177
	v_pk_mul_f32 v[140:141], v[142:143], v[140:141]
	v_mul_f32_e32 v144, 0xbfb8aa3b, v144
	v_mul_f32_e32 v145, 0xbfb8aa3b, v145
	v_pk_mul_f32 v[104:105], v[104:105], v[140:141]
	s_waitcnt vmcnt(17)
	v_cvt_pk_f32_fp8_e32 v[140:141], v138
	v_exp_f32_e32 v144, v144
	v_exp_f32_e32 v145, v145
	v_add_f32_e32 v147, 1.0, v147
	v_rcp_f32_e32 v147, v147
	v_pk_add_f32 v[144:145], v[144:145], 1.0 op_sel_hi:[1,0]
	v_med3_f32 v140, v140, s35, v177
	v_pk_mul_f32 v[144:145], v[146:147], v[144:145]
	s_waitcnt vmcnt(16)
	v_cvt_pk_f32_fp8_e32 v[146:147], v136
	v_mul_f32_e32 v140, 0xbfb8aa3b, v140
	v_exp_f32_e32 v152, v140
	v_cvt_pk_f32_fp8_sdwa v[142:143], v138 src0_sel:WORD_1
	v_med3_f32 v141, v141, s35, v177
	v_mul_f32_e32 v141, 0xbfb8aa3b, v141
	v_med3_f32 v140, v146, s35, v177
	v_add_f32_e32 v146, 1.0, v152
	v_exp_f32_e32 v152, v141
	v_med3_f32 v142, v142, s35, v177
	v_cvt_pk_f32_fp8_sdwa v[148:149], v136 src0_sel:WORD_1
	v_mul_f32_e32 v142, 0xbfb8aa3b, v142
	v_med3_f32 v141, v147, s35, v177
	v_add_f32_e32 v147, 1.0, v152
	v_exp_f32_e32 v152, v142
	v_med3_f32 v143, v143, s35, v177
	v_mul_f32_e32 v140, 0xbfb8aa3b, v140
	v_mul_f32_e32 v141, 0xbfb8aa3b, v141
	v_mul_f32_e32 v143, 0xbfb8aa3b, v143
	v_exp_f32_e32 v140, v140
	v_exp_f32_e32 v141, v141
	v_med3_f32 v142, v148, s35, v177
	v_add_f32_e32 v148, 1.0, v152
	v_exp_f32_e32 v152, v143
	v_rcp_f32_e32 v146, v146
	v_rcp_f32_e32 v147, v147
	v_pk_mul_f32 v[102:103], v[102:103], v[144:145]
	v_cvt_pk_f32_fp8_e32 v[144:145], v139
	v_med3_f32 v149, v149, s35, v177
	v_mul_f32_e32 v142, 0xbfb8aa3b, v142
	v_mul_f32_e32 v143, 0xbfb8aa3b, v149
	v_exp_f32_e32 v142, v142
	v_exp_f32_e32 v143, v143
	v_add_f32_e32 v149, 1.0, v152
	v_pk_add_f32 v[140:141], v[140:141], 1.0 op_sel_hi:[1,0]
	v_rcp_f32_e32 v148, v148
	v_rcp_f32_e32 v149, v149
	v_pk_mul_f32 v[140:141], v[146:147], v[140:141]
	v_cvt_pk_f32_fp8_sdwa v[138:139], v139 src0_sel:WORD_1
	v_pk_mul_f32 v[106:107], v[106:107], v[140:141]
	v_med3_f32 v141, v144, s35, v177
	v_pk_add_f32 v[142:143], v[142:143], 1.0 op_sel_hi:[1,0]
	v_mul_f32_e32 v141, 0xbfb8aa3b, v141
	v_pk_mul_f32 v[142:143], v[148:149], v[142:143]
	v_exp_f32_e32 v141, v141
	v_cvt_pk_f32_fp8_e32 v[150:151], v137
	v_cvt_pk_f32_fp8_sdwa v[136:137], v137 src0_sel:WORD_1
	v_pk_mul_f32 v[108:109], v[108:109], v[142:143]
	v_med3_f32 v143, v145, s35, v177
	v_med3_f32 v138, v138, s35, v177
	v_med3_f32 v139, v139, s35, v177
	v_mul_f32_e32 v143, 0xbfb8aa3b, v143
	v_mul_f32_e32 v138, 0xbfb8aa3b, v138
	v_mul_f32_e32 v139, 0xbfb8aa3b, v139
	v_add_f32_e32 v141, 1.0, v141
	v_exp_f32_e32 v143, v143
	v_exp_f32_e32 v138, v138
	v_exp_f32_e32 v139, v139
	v_rcp_f32_e32 v142, v141
	v_med3_f32 v140, v150, s35, v177
	v_med3_f32 v141, v151, s35, v177
	v_med3_f32 v136, v136, s35, v177
	v_med3_f32 v137, v137, s35, v177
	v_mul_f32_e32 v140, 0xbfb8aa3b, v140
	v_mul_f32_e32 v141, 0xbfb8aa3b, v141
	v_mul_f32_e32 v136, 0xbfb8aa3b, v136
	v_mul_f32_e32 v137, 0xbfb8aa3b, v137
	v_exp_f32_e32 v140, v140
	v_exp_f32_e32 v141, v141
	v_add_f32_e32 v143, 1.0, v143
	v_exp_f32_e32 v136, v136
	v_add_f32_e32 v138, 1.0, v138
	v_exp_f32_e32 v137, v137
	v_add_f32_e32 v139, 1.0, v139
	v_rcp_f32_e32 v143, v143
	v_rcp_f32_e32 v138, v138
	v_rcp_f32_e32 v139, v139
	v_pk_add_f32 v[136:137], v[136:137], 1.0 op_sel_hi:[1,0]
	v_pk_add_f32 v[140:141], v[140:141], 1.0 op_sel_hi:[1,0]
	v_pk_mul_f32 v[136:137], v[138:139], v[136:137]
	v_pk_mul_f32 v[140:141], v[142:143], v[140:141]
	v_pk_mul_f32 v[116:117], v[116:117], v[136:137]
	v_pk_mul_f32 v[114:115], v[114:115], v[140:141]
	s_nop 0
	s_waitcnt vmcnt(0)
	v_mov_b64_e32 v[162:163], v[220:221]
	v_mov_b64_e32 v[160:161], v[222:223]
	v_mov_b64_e32 v[178:179], v[224:225]
	v_mov_b64_e32 v[180:181], v[226:227]
	v_mov_b64_e32 v[158:159], v[228:229]
	v_mov_b64_e32 v[156:157], v[230:231]
	v_mov_b64_e32 v[154:155], v[232:233]
	v_mov_b64_e32 v[152:153], v[234:235]
	v_mov_b64_e32 v[150:151], v[236:237]
	v_mov_b64_e32 v[148:149], v[238:239]
	v_mov_b64_e32 v[146:147], v[240:241]
	v_mov_b64_e32 v[144:145], v[242:243]
	v_mov_b64_e32 v[142:143], v[244:245]
	v_mov_b64_e32 v[140:141], v[246:247]
	v_mov_b64_e32 v[138:139], v[248:249]
	v_mov_b64_e32 v[136:137], v[250:251]
	s_waitcnt vmcnt(15)
	v_cvt_pk_f32_fp8_e32 v[182:183], v162
	s_waitcnt vmcnt(14)
	v_cvt_pk_f32_fp8_e32 v[188:189], v160
	v_cvt_pk_f32_fp8_sdwa v[184:185], v162 src0_sel:WORD_1
	v_cvt_pk_f32_fp8_sdwa v[190:191], v160 src0_sel:WORD_1
	v_med3_f32 v182, v182, s35, v177
	v_mul_f32_e32 v182, 0xbfb8aa3b, v182
	v_max_f32_e32 v134, v188, v188
	v_exp_f32_e32 v188, v182
	v_med3_f32 v134, v134, s35, v177
	v_mul_f32_e32 v134, 0xbfb8aa3b, v134
	v_med3_f32 v183, v183, s35, v177
	v_exp_f32_e32 v182, v134
	v_add_f32_e32 v134, 1.0, v188
	v_mul_f32_e32 v183, 0xbfb8aa3b, v183
	v_rcp_f32_e32 v188, v134
	v_max_f32_e32 v134, v189, v189
	v_exp_f32_e32 v189, v183
	v_med3_f32 v134, v134, s35, v177
	v_mul_f32_e32 v134, 0xbfb8aa3b, v134
	v_med3_f32 v184, v184, s35, v177
	v_exp_f32_e32 v183, v134
	v_add_f32_e32 v134, 1.0, v189
	v_mul_f32_e32 v184, 0xbfb8aa3b, v184
	v_rcp_f32_e32 v189, v134
	v_max_f32_e32 v134, v190, v190
	v_exp_f32_e32 v190, v184
	v_cvt_pk_f32_fp8_e32 v[186:187], v163
	v_med3_f32 v134, v134, s35, v177
	v_med3_f32 v185, v185, s35, v177
	v_mul_f32_e32 v134, 0xbfb8aa3b, v134
	v_mul_f32_e32 v185, 0xbfb8aa3b, v185
	v_pk_add_f32 v[182:183], v[182:183], 1.0 op_sel_hi:[1,0]
	v_exp_f32_e32 v184, v134
	v_add_f32_e32 v134, 1.0, v190
	v_max_f32_e32 v190, v191, v191
	v_exp_f32_e32 v191, v185
	v_pk_mul_f32 v[182:183], v[188:189], v[182:183]
	v_cvt_pk_f32_fp8_e32 v[192:193], v161
	v_pk_mul_f32 v[118:119], v[118:119], v[182:183]
	v_med3_f32 v182, v186, s35, v177
	v_med3_f32 v190, v190, s35, v177
	v_mul_f32_e32 v182, 0xbfb8aa3b, v182
	v_mul_f32_e32 v185, 0xbfb8aa3b, v190
	v_rcp_f32_e32 v190, v134
	v_add_f32_e32 v134, 1.0, v191
	v_exp_f32_e32 v183, v182
	v_exp_f32_e32 v185, v185
	v_rcp_f32_e32 v191, v134
	v_med3_f32 v134, v192, s35, v177
	v_mul_f32_e32 v134, 0xbfb8aa3b, v134
	v_exp_f32_e32 v182, v134
	v_add_f32_e32 v134, 1.0, v183
	v_pk_add_f32 v[184:185], v[184:185], 1.0 op_sel_hi:[1,0]
	v_med3_f32 v183, v187, s35, v177
	v_pk_mul_f32 v[184:185], v[190:191], v[184:185]
	v_mul_f32_e32 v183, 0xbfb8aa3b, v183
	v_pk_mul_f32 v[120:121], v[120:121], v[184:185]
	v_exp_f32_e32 v185, v183
	v_cvt_pk_f32_fp8_sdwa v[162:163], v163 src0_sel:WORD_1
	v_cvt_pk_f32_fp8_sdwa v[160:161], v161 src0_sel:WORD_1
	v_rcp_f32_e32 v184, v134
	v_med3_f32 v134, v193, s35, v177
	v_mul_f32_e32 v134, 0xbfb8aa3b, v134
	v_exp_f32_e32 v183, v134
	v_add_f32_e32 v134, 1.0, v185
	v_rcp_f32_e32 v185, v134
	v_max_f32_e32 v134, v160, v160
	v_med3_f32 v160, v162, s35, v177
	v_mul_f32_e32 v160, 0xbfb8aa3b, v160
	v_exp_f32_e32 v162, v160
	v_med3_f32 v134, v134, s35, v177
	v_mul_f32_e32 v134, 0xbfb8aa3b, v134
	v_exp_f32_e32 v160, v134
	v_add_f32_e32 v134, 1.0, v162
	v_med3_f32 v162, v163, s35, v177
	v_mul_f32_e32 v162, 0xbfb8aa3b, v162
	v_exp_f32_e32 v163, v162
	v_med3_f32 v161, v161, s35, v177
	v_mul_f32_e32 v161, 0xbfb8aa3b, v161
	v_exp_f32_e32 v161, v161
	v_rcp_f32_e32 v162, v134
	v_add_f32_e32 v134, 1.0, v163
	v_rcp_f32_e32 v163, v134
	v_pk_add_f32 v[160:161], v[160:161], 1.0 op_sel_hi:[1,0]
	v_pk_add_f32 v[182:183], v[182:183], 1.0 op_sel_hi:[1,0]
	s_waitcnt vmcnt(12)
	v_cvt_pk_f32_fp8_sdwa v[186:187], v180 src0_sel:WORD_1
	v_pk_mul_f32 v[160:161], v[162:163], v[160:161]
	v_pk_mul_f32 v[182:183], v[184:185], v[182:183]
	v_pk_mul_f32 v[128:129], v[128:129], v[160:161]
	v_cvt_pk_f32_fp8_e32 v[160:161], v178
	v_cvt_pk_f32_fp8_e32 v[184:185], v180
	v_cvt_pk_f32_fp8_sdwa v[162:163], v178 src0_sel:WORD_1
	v_pk_mul_f32 v[126:127], v[126:127], v[182:183]
	v_med3_f32 v160, v160, s35, v177
	v_mul_f32_e32 v160, 0xbfb8aa3b, v160
	v_max_f32_e32 v134, v184, v184
	v_exp_f32_e32 v184, v160
	v_med3_f32 v134, v134, s35, v177
	v_mul_f32_e32 v134, 0xbfb8aa3b, v134
	v_med3_f32 v161, v161, s35, v177
	v_exp_f32_e32 v160, v134
	v_add_f32_e32 v134, 1.0, v184
	v_mul_f32_e32 v161, 0xbfb8aa3b, v161
	v_rcp_f32_e32 v184, v134
	v_max_f32_e32 v134, v185, v185
	v_exp_f32_e32 v185, v161
	v_med3_f32 v134, v134, s35, v177
	v_mul_f32_e32 v134, 0xbfb8aa3b, v134
	v_med3_f32 v162, v162, s35, v177
	v_exp_f32_e32 v161, v134
	v_add_f32_e32 v134, 1.0, v185
	v_mul_f32_e32 v162, 0xbfb8aa3b, v162
	v_rcp_f32_e32 v185, v134
	v_max_f32_e32 v134, v186, v186
	v_exp_f32_e32 v186, v162
	v_cvt_pk_f32_fp8_e32 v[182:183], v179
	v_med3_f32 v134, v134, s35, v177
	v_med3_f32 v163, v163, s35, v177
	v_mul_f32_e32 v134, 0xbfb8aa3b, v134
	v_mul_f32_e32 v163, 0xbfb8aa3b, v163
	v_pk_add_f32 v[160:161], v[160:161], 1.0 op_sel_hi:[1,0]
	v_exp_f32_e32 v162, v134
	v_add_f32_e32 v134, 1.0, v186
	v_max_f32_e32 v186, v187, v187
	v_exp_f32_e32 v187, v163
	v_pk_mul_f32 v[160:161], v[184:185], v[160:161]
	v_cvt_pk_f32_fp8_e32 v[188:189], v181
	v_pk_mul_f32 v[122:123], v[122:123], v[160:161]
	v_med3_f32 v160, v182, s35, v177
	v_med3_f32 v186, v186, s35, v177
	v_mul_f32_e32 v160, 0xbfb8aa3b, v160
	v_mul_f32_e32 v163, 0xbfb8aa3b, v186
	v_rcp_f32_e32 v186, v134
	v_add_f32_e32 v134, 1.0, v187
	v_exp_f32_e32 v161, v160
	v_exp_f32_e32 v163, v163
	v_rcp_f32_e32 v187, v134
	v_med3_f32 v134, v188, s35, v177
	v_mul_f32_e32 v134, 0xbfb8aa3b, v134
	v_exp_f32_e32 v160, v134
	v_add_f32_e32 v134, 1.0, v161
	v_cvt_pk_f32_fp8_sdwa v[178:179], v179 src0_sel:WORD_1
	v_pk_add_f32 v[162:163], v[162:163], 1.0 op_sel_hi:[1,0]
	v_med3_f32 v161, v183, s35, v177
	v_pk_mul_f32 v[162:163], v[186:187], v[162:163]
	v_mul_f32_e32 v161, 0xbfb8aa3b, v161
	v_pk_mul_f32 v[124:125], v[124:125], v[162:163]
	v_exp_f32_e32 v163, v161
	v_cvt_pk_f32_fp8_sdwa v[180:181], v181 src0_sel:WORD_1
	v_rcp_f32_e32 v162, v134
	v_med3_f32 v134, v189, s35, v177
	v_mul_f32_e32 v134, 0xbfb8aa3b, v134
	v_med3_f32 v178, v178, s35, v177
	v_exp_f32_e32 v161, v134
	v_add_f32_e32 v134, 1.0, v163
	v_mul_f32_e32 v178, 0xbfb8aa3b, v178
	v_rcp_f32_e32 v163, v134
	v_max_f32_e32 v134, v180, v180
	v_exp_f32_e32 v180, v178
	v_med3_f32 v134, v134, s35, v177
	v_med3_f32 v179, v179, s35, v177
	v_mul_f32_e32 v134, 0xbfb8aa3b, v134
	v_mul_f32_e32 v179, 0xbfb8aa3b, v179
	v_exp_f32_e32 v178, v134
	v_add_f32_e32 v134, 1.0, v180
	v_max_f32_e32 v180, v181, v181
	v_exp_f32_e32 v181, v179
	v_med3_f32 v180, v180, s35, v177
	v_mul_f32_e32 v179, 0xbfb8aa3b, v180
	v_exp_f32_e32 v179, v179
	v_rcp_f32_e32 v180, v134
	v_add_f32_e32 v134, 1.0, v181
	v_pk_add_f32 v[160:161], v[160:161], 1.0 op_sel_hi:[1,0]
	v_rcp_f32_e32 v181, v134
	v_pk_mul_f32 v[160:161], v[162:163], v[160:161]
	v_pk_add_f32 v[178:179], v[178:179], 1.0 op_sel_hi:[1,0]
	v_pk_mul_f32 v[110:111], v[110:111], v[160:161]
	s_waitcnt vmcnt(11)
	v_cvt_pk_f32_fp8_e32 v[160:161], v158
	v_pk_mul_f32 v[162:163], v[180:181], v[178:179]
	s_waitcnt vmcnt(10)
	v_cvt_pk_f32_fp8_e32 v[180:181], v156
	v_pk_mul_f32 v[112:113], v[112:113], v[162:163]
	v_med3_f32 v160, v160, s35, v177
	v_mul_f32_e32 v160, 0xbfb8aa3b, v160
	v_max_f32_e32 v134, v180, v180
	v_exp_f32_e32 v180, v160
	v_med3_f32 v134, v134, s35, v177
	v_cvt_pk_f32_fp8_sdwa v[162:163], v158 src0_sel:WORD_1
	v_mul_f32_e32 v134, 0xbfb8aa3b, v134
	v_med3_f32 v161, v161, s35, v177
	v_exp_f32_e32 v160, v134
	v_add_f32_e32 v134, 1.0, v180
	v_mul_f32_e32 v161, 0xbfb8aa3b, v161
	v_rcp_f32_e32 v180, v134
	v_max_f32_e32 v134, v181, v181
	v_exp_f32_e32 v181, v161
	v_cvt_pk_f32_fp8_sdwa v[182:183], v156 src0_sel:WORD_1
	v_med3_f32 v134, v134, s35, v177
	v_mul_f32_e32 v134, 0xbfb8aa3b, v134
	v_med3_f32 v162, v162, s35, v177
	v_exp_f32_e32 v161, v134
	v_add_f32_e32 v134, 1.0, v181
	v_mul_f32_e32 v162, 0xbfb8aa3b, v162
	v_rcp_f32_e32 v181, v134
	v_max_f32_e32 v134, v182, v182
	v_exp_f32_e32 v182, v162
	v_cvt_pk_f32_fp8_e32 v[178:179], v159
	v_med3_f32 v134, v134, s35, v177
	v_med3_f32 v163, v163, s35, v177
	v_mul_f32_e32 v134, 0xbfb8aa3b, v134
	v_mul_f32_e32 v163, 0xbfb8aa3b, v163
	v_pk_add_f32 v[160:161], v[160:161], 1.0 op_sel_hi:[1,0]
	v_exp_f32_e32 v162, v134
	v_add_f32_e32 v134, 1.0, v182
	v_max_f32_e32 v182, v183, v183
	v_exp_f32_e32 v183, v163
	v_pk_mul_f32 v[160:161], v[180:181], v[160:161]
	v_cvt_pk_f32_fp8_e32 v[184:185], v157
	v_pk_mul_f32 v[98:99], v[98:99], v[160:161]
	v_med3_f32 v160, v178, s35, v177
	v_med3_f32 v182, v182, s35, v177
	v_mul_f32_e32 v160, 0xbfb8aa3b, v160
	v_mul_f32_e32 v163, 0xbfb8aa3b, v182
	v_rcp_f32_e32 v182, v134
	v_add_f32_e32 v134, 1.0, v183
	v_exp_f32_e32 v161, v160
	v_exp_f32_e32 v163, v163
	v_rcp_f32_e32 v183, v134
	v_med3_f32 v134, v184, s35, v177
	v_mul_f32_e32 v134, 0xbfb8aa3b, v134
	v_exp_f32_e32 v160, v134
	v_add_f32_e32 v134, 1.0, v161
	v_pk_add_f32 v[162:163], v[162:163], 1.0 op_sel_hi:[1,0]
	v_med3_f32 v161, v179, s35, v177
	v_pk_mul_f32 v[162:163], v[182:183], v[162:163]
	v_mul_f32_e32 v161, 0xbfb8aa3b, v161
	v_pk_mul_f32 v[100:101], v[100:101], v[162:163]
	v_exp_f32_e32 v163, v161
	v_cvt_pk_f32_fp8_sdwa v[158:159], v159 src0_sel:WORD_1
	v_cvt_pk_f32_fp8_sdwa v[156:157], v157 src0_sel:WORD_1
	v_rcp_f32_e32 v162, v134
	v_med3_f32 v134, v185, s35, v177
	v_mul_f32_e32 v134, 0xbfb8aa3b, v134
	v_exp_f32_e32 v161, v134
	v_add_f32_e32 v134, 1.0, v163
	v_rcp_f32_e32 v163, v134
	v_max_f32_e32 v134, v156, v156
	v_med3_f32 v156, v158, s35, v177
	v_mul_f32_e32 v156, 0xbfb8aa3b, v156
	v_exp_f32_e32 v158, v156
	v_med3_f32 v134, v134, s35, v177
	v_mul_f32_e32 v134, 0xbfb8aa3b, v134
	v_exp_f32_e32 v156, v134
	v_add_f32_e32 v134, 1.0, v158
	v_med3_f32 v158, v159, s35, v177
	v_mul_f32_e32 v158, 0xbfb8aa3b, v158
	v_exp_f32_e32 v159, v158
	v_med3_f32 v157, v157, s35, v177
	v_mul_f32_e32 v157, 0xbfb8aa3b, v157
	v_exp_f32_e32 v157, v157
	v_rcp_f32_e32 v158, v134
	v_add_f32_e32 v134, 1.0, v159
	v_rcp_f32_e32 v159, v134
	v_pk_add_f32 v[156:157], v[156:157], 1.0 op_sel_hi:[1,0]
	v_pk_add_f32 v[160:161], v[160:161], 1.0 op_sel_hi:[1,0]
	s_waitcnt vmcnt(8)
	v_cvt_pk_f32_fp8_sdwa v[178:179], v152 src0_sel:WORD_1
	v_pk_mul_f32 v[156:157], v[158:159], v[156:157]
	v_pk_mul_f32 v[160:161], v[162:163], v[160:161]
	v_pk_mul_f32 v[88:89], v[88:89], v[156:157]
	v_cvt_pk_f32_fp8_e32 v[156:157], v154
	v_cvt_pk_f32_fp8_e32 v[162:163], v152
	v_cvt_pk_f32_fp8_sdwa v[158:159], v154 src0_sel:WORD_1
	v_pk_mul_f32 v[86:87], v[86:87], v[160:161]
	v_med3_f32 v156, v156, s35, v177
	v_mul_f32_e32 v156, 0xbfb8aa3b, v156
	v_max_f32_e32 v134, v162, v162
	v_exp_f32_e32 v162, v156
	v_med3_f32 v134, v134, s35, v177
	v_mul_f32_e32 v134, 0xbfb8aa3b, v134
	v_med3_f32 v157, v157, s35, v177
	v_exp_f32_e32 v156, v134
	v_add_f32_e32 v134, 1.0, v162
	v_mul_f32_e32 v157, 0xbfb8aa3b, v157
	v_rcp_f32_e32 v162, v134
	v_max_f32_e32 v134, v163, v163
	v_exp_f32_e32 v163, v157
	v_med3_f32 v134, v134, s35, v177
	v_mul_f32_e32 v134, 0xbfb8aa3b, v134
	v_med3_f32 v158, v158, s35, v177
	v_exp_f32_e32 v157, v134
	v_add_f32_e32 v134, 1.0, v163
	v_mul_f32_e32 v158, 0xbfb8aa3b, v158
	v_rcp_f32_e32 v163, v134
	v_max_f32_e32 v134, v178, v178
	v_exp_f32_e32 v178, v158
	v_cvt_pk_f32_fp8_e32 v[160:161], v155
	v_med3_f32 v134, v134, s35, v177
	v_med3_f32 v159, v159, s35, v177
	v_mul_f32_e32 v134, 0xbfb8aa3b, v134
	v_mul_f32_e32 v159, 0xbfb8aa3b, v159
	v_pk_add_f32 v[156:157], v[156:157], 1.0 op_sel_hi:[1,0]
	v_exp_f32_e32 v158, v134
	v_add_f32_e32 v134, 1.0, v178
	v_max_f32_e32 v178, v179, v179
	v_exp_f32_e32 v179, v159
	v_pk_mul_f32 v[156:157], v[162:163], v[156:157]
	v_cvt_pk_f32_fp8_e32 v[180:181], v153
	v_pk_mul_f32 v[70:71], v[70:71], v[156:157]
	v_med3_f32 v156, v160, s35, v177
	v_med3_f32 v178, v178, s35, v177
	v_mul_f32_e32 v156, 0xbfb8aa3b, v156
	v_mul_f32_e32 v159, 0xbfb8aa3b, v178
	v_rcp_f32_e32 v178, v134
	v_add_f32_e32 v134, 1.0, v179
	v_exp_f32_e32 v157, v156
	v_exp_f32_e32 v159, v159
	v_rcp_f32_e32 v179, v134
	v_med3_f32 v134, v180, s35, v177
	v_mul_f32_e32 v134, 0xbfb8aa3b, v134
	v_exp_f32_e32 v156, v134
	v_add_f32_e32 v134, 1.0, v157
	v_pk_add_f32 v[158:159], v[158:159], 1.0 op_sel_hi:[1,0]
	v_med3_f32 v157, v161, s35, v177
	v_pk_mul_f32 v[158:159], v[178:179], v[158:159]
	v_mul_f32_e32 v157, 0xbfb8aa3b, v157
	v_pk_mul_f32 v[72:73], v[72:73], v[158:159]
	v_exp_f32_e32 v159, v157
	v_cvt_pk_f32_fp8_sdwa v[154:155], v155 src0_sel:WORD_1
	v_cvt_pk_f32_fp8_sdwa v[152:153], v153 src0_sel:WORD_1
	v_rcp_f32_e32 v158, v134
	v_med3_f32 v134, v181, s35, v177
	v_mul_f32_e32 v134, 0xbfb8aa3b, v134
	v_exp_f32_e32 v157, v134
	v_add_f32_e32 v134, 1.0, v159
	v_rcp_f32_e32 v159, v134
	v_max_f32_e32 v134, v152, v152
	v_med3_f32 v152, v154, s35, v177
	v_mul_f32_e32 v152, 0xbfb8aa3b, v152
	v_exp_f32_e32 v154, v152
	v_med3_f32 v134, v134, s35, v177
	v_mul_f32_e32 v134, 0xbfb8aa3b, v134
	v_exp_f32_e32 v152, v134
	v_add_f32_e32 v134, 1.0, v154
	v_med3_f32 v154, v155, s35, v177
	v_mul_f32_e32 v154, 0xbfb8aa3b, v154
	v_exp_f32_e32 v155, v154
	v_med3_f32 v153, v153, s35, v177
	v_mul_f32_e32 v153, 0xbfb8aa3b, v153
	v_exp_f32_e32 v153, v153
	v_rcp_f32_e32 v154, v134
	v_add_f32_e32 v134, 1.0, v155
	v_rcp_f32_e32 v155, v134
	v_pk_add_f32 v[152:153], v[152:153], 1.0 op_sel_hi:[1,0]
	v_pk_add_f32 v[156:157], v[156:157], 1.0 op_sel_hi:[1,0]
	s_waitcnt vmcnt(6)
	v_cvt_pk_f32_fp8_sdwa v[160:161], v148 src0_sel:WORD_1
	v_pk_mul_f32 v[152:153], v[154:155], v[152:153]
	v_pk_mul_f32 v[156:157], v[158:159], v[156:157]
	v_pk_mul_f32 v[60:61], v[60:61], v[152:153]
	v_cvt_pk_f32_fp8_e32 v[152:153], v150
	v_cvt_pk_f32_fp8_e32 v[158:159], v148
	v_cvt_pk_f32_fp8_sdwa v[154:155], v150 src0_sel:WORD_1
	v_pk_mul_f32 v[58:59], v[58:59], v[156:157]
	v_med3_f32 v152, v152, s35, v177
	v_mul_f32_e32 v152, 0xbfb8aa3b, v152
	v_max_f32_e32 v134, v158, v158
	v_exp_f32_e32 v158, v152
	v_med3_f32 v134, v134, s35, v177
	v_mul_f32_e32 v134, 0xbfb8aa3b, v134
	v_med3_f32 v153, v153, s35, v177
	v_exp_f32_e32 v152, v134
	v_add_f32_e32 v134, 1.0, v158
	v_mul_f32_e32 v153, 0xbfb8aa3b, v153
	v_rcp_f32_e32 v158, v134
	v_max_f32_e32 v134, v159, v159
	v_exp_f32_e32 v159, v153
	v_med3_f32 v134, v134, s35, v177
	v_mul_f32_e32 v134, 0xbfb8aa3b, v134
	v_med3_f32 v154, v154, s35, v177
	v_exp_f32_e32 v153, v134
	v_add_f32_e32 v134, 1.0, v159
	v_mul_f32_e32 v154, 0xbfb8aa3b, v154
	v_rcp_f32_e32 v159, v134
	v_max_f32_e32 v134, v160, v160
	v_exp_f32_e32 v160, v154
	v_cvt_pk_f32_fp8_e32 v[156:157], v151
	v_med3_f32 v134, v134, s35, v177
	v_med3_f32 v155, v155, s35, v177
	v_mul_f32_e32 v134, 0xbfb8aa3b, v134
	v_mul_f32_e32 v155, 0xbfb8aa3b, v155
	v_pk_add_f32 v[152:153], v[152:153], 1.0 op_sel_hi:[1,0]
	v_exp_f32_e32 v154, v134
	v_add_f32_e32 v134, 1.0, v160
	v_max_f32_e32 v160, v161, v161
	v_exp_f32_e32 v161, v155
	v_pk_mul_f32 v[152:153], v[158:159], v[152:153]
	v_cvt_pk_f32_fp8_e32 v[162:163], v149
	v_pk_mul_f32 v[46:47], v[46:47], v[152:153]
	v_med3_f32 v152, v156, s35, v177
	v_med3_f32 v160, v160, s35, v177
	v_mul_f32_e32 v152, 0xbfb8aa3b, v152
	v_mul_f32_e32 v155, 0xbfb8aa3b, v160
	v_rcp_f32_e32 v160, v134
	v_add_f32_e32 v134, 1.0, v161
	v_exp_f32_e32 v153, v152
	v_exp_f32_e32 v155, v155
	v_rcp_f32_e32 v161, v134
	v_med3_f32 v134, v162, s35, v177
	v_mul_f32_e32 v134, 0xbfb8aa3b, v134
	v_exp_f32_e32 v152, v134
	v_add_f32_e32 v134, 1.0, v153
	v_pk_add_f32 v[154:155], v[154:155], 1.0 op_sel_hi:[1,0]
	v_med3_f32 v153, v157, s35, v177
	v_pk_mul_f32 v[154:155], v[160:161], v[154:155]
	v_mul_f32_e32 v153, 0xbfb8aa3b, v153
	v_pk_mul_f32 v[48:49], v[48:49], v[154:155]
	v_exp_f32_e32 v155, v153
	v_cvt_pk_f32_fp8_sdwa v[150:151], v151 src0_sel:WORD_1
	v_cvt_pk_f32_fp8_sdwa v[148:149], v149 src0_sel:WORD_1
	v_rcp_f32_e32 v154, v134
	v_med3_f32 v134, v163, s35, v177
	v_mul_f32_e32 v134, 0xbfb8aa3b, v134
	v_exp_f32_e32 v153, v134
	v_add_f32_e32 v134, 1.0, v155
	v_rcp_f32_e32 v155, v134
	v_max_f32_e32 v134, v148, v148
	v_med3_f32 v148, v150, s35, v177
	v_mul_f32_e32 v148, 0xbfb8aa3b, v148
	v_exp_f32_e32 v150, v148
	v_med3_f32 v134, v134, s35, v177
	v_mul_f32_e32 v134, 0xbfb8aa3b, v134
	v_exp_f32_e32 v148, v134
	v_add_f32_e32 v134, 1.0, v150
	v_med3_f32 v150, v151, s35, v177
	v_mul_f32_e32 v150, 0xbfb8aa3b, v150
	v_exp_f32_e32 v151, v150
	v_med3_f32 v149, v149, s35, v177
	v_mul_f32_e32 v149, 0xbfb8aa3b, v149
	v_exp_f32_e32 v149, v149
	v_rcp_f32_e32 v150, v134
	v_add_f32_e32 v134, 1.0, v151
	v_rcp_f32_e32 v151, v134
	v_pk_add_f32 v[148:149], v[148:149], 1.0 op_sel_hi:[1,0]
	v_pk_add_f32 v[152:153], v[152:153], 1.0 op_sel_hi:[1,0]
	s_waitcnt vmcnt(4)
	v_cvt_pk_f32_fp8_sdwa v[156:157], v144 src0_sel:WORD_1
	v_pk_mul_f32 v[148:149], v[150:151], v[148:149]
	v_pk_mul_f32 v[152:153], v[154:155], v[152:153]
	v_pk_mul_f32 v[36:37], v[36:37], v[148:149]
	v_cvt_pk_f32_fp8_e32 v[148:149], v146
	v_cvt_pk_f32_fp8_e32 v[154:155], v144
	v_cvt_pk_f32_fp8_sdwa v[150:151], v146 src0_sel:WORD_1
	v_pk_mul_f32 v[34:35], v[34:35], v[152:153]
	v_med3_f32 v148, v148, s35, v177
	v_mul_f32_e32 v148, 0xbfb8aa3b, v148
	v_max_f32_e32 v134, v154, v154
	v_exp_f32_e32 v154, v148
	v_med3_f32 v134, v134, s35, v177
	v_mul_f32_e32 v134, 0xbfb8aa3b, v134
	v_med3_f32 v149, v149, s35, v177
	v_exp_f32_e32 v148, v134
	v_add_f32_e32 v134, 1.0, v154
	v_mul_f32_e32 v149, 0xbfb8aa3b, v149
	v_rcp_f32_e32 v154, v134
	v_max_f32_e32 v134, v155, v155
	v_exp_f32_e32 v155, v149
	v_med3_f32 v134, v134, s35, v177
	v_mul_f32_e32 v134, 0xbfb8aa3b, v134
	v_med3_f32 v150, v150, s35, v177
	v_exp_f32_e32 v149, v134
	v_add_f32_e32 v134, 1.0, v155
	v_mul_f32_e32 v150, 0xbfb8aa3b, v150
	v_rcp_f32_e32 v155, v134
	v_max_f32_e32 v134, v156, v156
	v_exp_f32_e32 v156, v150
	v_cvt_pk_f32_fp8_e32 v[152:153], v147
	v_med3_f32 v134, v134, s35, v177
	v_med3_f32 v151, v151, s35, v177
	v_mul_f32_e32 v134, 0xbfb8aa3b, v134
	v_mul_f32_e32 v151, 0xbfb8aa3b, v151
	v_pk_add_f32 v[148:149], v[148:149], 1.0 op_sel_hi:[1,0]
	v_exp_f32_e32 v150, v134
	v_add_f32_e32 v134, 1.0, v156
	v_max_f32_e32 v156, v157, v157
	v_exp_f32_e32 v157, v151
	v_pk_mul_f32 v[148:149], v[154:155], v[148:149]
	v_cvt_pk_f32_fp8_e32 v[158:159], v145
	v_pk_mul_f32 v[22:23], v[22:23], v[148:149]
	v_med3_f32 v148, v152, s35, v177
	v_med3_f32 v156, v156, s35, v177
	v_mul_f32_e32 v148, 0xbfb8aa3b, v148
	v_mul_f32_e32 v151, 0xbfb8aa3b, v156
	v_rcp_f32_e32 v156, v134
	v_add_f32_e32 v134, 1.0, v157
	v_exp_f32_e32 v149, v148
	v_exp_f32_e32 v151, v151
	v_rcp_f32_e32 v157, v134
	v_med3_f32 v134, v158, s35, v177
	v_mul_f32_e32 v134, 0xbfb8aa3b, v134
	v_exp_f32_e32 v148, v134
	v_add_f32_e32 v134, 1.0, v149
	v_pk_add_f32 v[150:151], v[150:151], 1.0 op_sel_hi:[1,0]
	v_med3_f32 v149, v153, s35, v177
	v_pk_mul_f32 v[150:151], v[156:157], v[150:151]
	v_mul_f32_e32 v149, 0xbfb8aa3b, v149
	v_pk_mul_f32 v[24:25], v[24:25], v[150:151]
	v_exp_f32_e32 v151, v149
	v_cvt_pk_f32_fp8_sdwa v[146:147], v147 src0_sel:WORD_1
	v_cvt_pk_f32_fp8_sdwa v[144:145], v145 src0_sel:WORD_1
	v_rcp_f32_e32 v150, v134
	v_med3_f32 v134, v159, s35, v177
	v_mul_f32_e32 v134, 0xbfb8aa3b, v134
	v_exp_f32_e32 v149, v134
	v_add_f32_e32 v134, 1.0, v151
	v_rcp_f32_e32 v151, v134
	v_max_f32_e32 v134, v144, v144
	v_med3_f32 v144, v146, s35, v177
	v_mul_f32_e32 v144, 0xbfb8aa3b, v144
	v_exp_f32_e32 v146, v144
	v_med3_f32 v134, v134, s35, v177
	v_mul_f32_e32 v134, 0xbfb8aa3b, v134
	v_exp_f32_e32 v144, v134
	v_add_f32_e32 v134, 1.0, v146
	v_med3_f32 v146, v147, s35, v177
	v_mul_f32_e32 v146, 0xbfb8aa3b, v146
	v_exp_f32_e32 v147, v146
	v_med3_f32 v145, v145, s35, v177
	v_mul_f32_e32 v145, 0xbfb8aa3b, v145
	v_exp_f32_e32 v145, v145
	v_rcp_f32_e32 v146, v134
	v_add_f32_e32 v134, 1.0, v147
	v_rcp_f32_e32 v147, v134
	v_pk_add_f32 v[144:145], v[144:145], 1.0 op_sel_hi:[1,0]
	v_pk_add_f32 v[148:149], v[148:149], 1.0 op_sel_hi:[1,0]
	s_waitcnt vmcnt(2)
	v_cvt_pk_f32_fp8_sdwa v[152:153], v140 src0_sel:WORD_1
	v_pk_mul_f32 v[144:145], v[146:147], v[144:145]
	v_pk_mul_f32 v[148:149], v[150:151], v[148:149]
	v_pk_mul_f32 v[20:21], v[20:21], v[144:145]
	v_cvt_pk_f32_fp8_e32 v[144:145], v142
	v_cvt_pk_f32_fp8_e32 v[150:151], v140
	v_cvt_pk_f32_fp8_sdwa v[146:147], v142 src0_sel:WORD_1
	v_pk_mul_f32 v[18:19], v[18:19], v[148:149]
	v_med3_f32 v144, v144, s35, v177
	v_mul_f32_e32 v144, 0xbfb8aa3b, v144
	v_max_f32_e32 v134, v150, v150
	v_exp_f32_e32 v150, v144
	v_med3_f32 v134, v134, s35, v177
	v_mul_f32_e32 v134, 0xbfb8aa3b, v134
	v_med3_f32 v145, v145, s35, v177
	v_exp_f32_e32 v144, v134
	v_add_f32_e32 v134, 1.0, v150
	v_mul_f32_e32 v145, 0xbfb8aa3b, v145
	v_rcp_f32_e32 v150, v134
	v_max_f32_e32 v134, v151, v151
	v_exp_f32_e32 v151, v145
	v_med3_f32 v134, v134, s35, v177
	v_mul_f32_e32 v134, 0xbfb8aa3b, v134
	v_med3_f32 v146, v146, s35, v177
	v_exp_f32_e32 v145, v134
	v_add_f32_e32 v134, 1.0, v151
	v_mul_f32_e32 v146, 0xbfb8aa3b, v146
	v_rcp_f32_e32 v151, v134
	v_max_f32_e32 v134, v152, v152
	v_exp_f32_e32 v152, v146
	v_cvt_pk_f32_fp8_e32 v[148:149], v143
	v_med3_f32 v134, v134, s35, v177
	v_med3_f32 v147, v147, s35, v177
	v_mul_f32_e32 v134, 0xbfb8aa3b, v134
	v_mul_f32_e32 v147, 0xbfb8aa3b, v147
	v_pk_add_f32 v[144:145], v[144:145], 1.0 op_sel_hi:[1,0]
	v_exp_f32_e32 v146, v134
	v_add_f32_e32 v134, 1.0, v152
	v_max_f32_e32 v152, v153, v153
	v_exp_f32_e32 v153, v147
	v_pk_mul_f32 v[144:145], v[150:151], v[144:145]
	v_cvt_pk_f32_fp8_e32 v[154:155], v141
	v_pk_mul_f32 v[14:15], v[14:15], v[144:145]
	v_med3_f32 v144, v148, s35, v177
	v_med3_f32 v152, v152, s35, v177
	v_mul_f32_e32 v144, 0xbfb8aa3b, v144
	v_mul_f32_e32 v147, 0xbfb8aa3b, v152
	v_rcp_f32_e32 v152, v134
	v_add_f32_e32 v134, 1.0, v153
	v_exp_f32_e32 v145, v144
	v_exp_f32_e32 v147, v147
	v_rcp_f32_e32 v153, v134
	v_med3_f32 v134, v154, s35, v177
	v_mul_f32_e32 v134, 0xbfb8aa3b, v134
	v_exp_f32_e32 v144, v134
	v_add_f32_e32 v134, 1.0, v145
	v_pk_add_f32 v[146:147], v[146:147], 1.0 op_sel_hi:[1,0]
	v_med3_f32 v145, v149, s35, v177
	v_pk_mul_f32 v[146:147], v[152:153], v[146:147]
	v_mul_f32_e32 v145, 0xbfb8aa3b, v145
	v_pk_mul_f32 v[16:17], v[16:17], v[146:147]
	v_exp_f32_e32 v147, v145
	v_cvt_pk_f32_fp8_sdwa v[142:143], v143 src0_sel:WORD_1
	v_cvt_pk_f32_fp8_sdwa v[140:141], v141 src0_sel:WORD_1
	v_rcp_f32_e32 v146, v134
	v_med3_f32 v134, v155, s35, v177
	v_mul_f32_e32 v134, 0xbfb8aa3b, v134
	v_exp_f32_e32 v145, v134
	v_add_f32_e32 v134, 1.0, v147
	v_rcp_f32_e32 v147, v134
	v_max_f32_e32 v134, v140, v140
	v_med3_f32 v140, v142, s35, v177
	v_mul_f32_e32 v140, 0xbfb8aa3b, v140
	v_exp_f32_e32 v142, v140
	v_med3_f32 v134, v134, s35, v177
	v_mul_f32_e32 v134, 0xbfb8aa3b, v134
	v_exp_f32_e32 v140, v134
	v_add_f32_e32 v134, 1.0, v142
	v_med3_f32 v142, v143, s35, v177
	v_mul_f32_e32 v142, 0xbfb8aa3b, v142
	v_exp_f32_e32 v143, v142
	v_med3_f32 v141, v141, s35, v177
	v_mul_f32_e32 v141, 0xbfb8aa3b, v141
	v_exp_f32_e32 v141, v141
	v_rcp_f32_e32 v142, v134
	v_add_f32_e32 v134, 1.0, v143
	v_rcp_f32_e32 v143, v134
	v_pk_add_f32 v[140:141], v[140:141], 1.0 op_sel_hi:[1,0]
	v_pk_add_f32 v[144:145], v[144:145], 1.0 op_sel_hi:[1,0]
	s_waitcnt vmcnt(0)
	v_cvt_pk_f32_fp8_sdwa v[148:149], v136 src0_sel:WORD_1
	v_pk_mul_f32 v[140:141], v[142:143], v[140:141]
	v_pk_mul_f32 v[144:145], v[146:147], v[144:145]
	v_pk_mul_f32 v[12:13], v[12:13], v[140:141]
	v_cvt_pk_f32_fp8_e32 v[140:141], v138
	v_cvt_pk_f32_fp8_e32 v[146:147], v136
	v_cvt_pk_f32_fp8_sdwa v[142:143], v138 src0_sel:WORD_1
	v_pk_mul_f32 v[10:11], v[10:11], v[144:145]
	v_med3_f32 v140, v140, s35, v177
	v_mul_f32_e32 v140, 0xbfb8aa3b, v140
	v_max_f32_e32 v134, v146, v146
	v_exp_f32_e32 v146, v140
	v_med3_f32 v134, v134, s35, v177
	v_mul_f32_e32 v134, 0xbfb8aa3b, v134
	v_med3_f32 v141, v141, s35, v177
	v_exp_f32_e32 v140, v134
	v_add_f32_e32 v134, 1.0, v146
	v_mul_f32_e32 v141, 0xbfb8aa3b, v141
	v_rcp_f32_e32 v146, v134
	v_max_f32_e32 v134, v147, v147
	v_exp_f32_e32 v147, v141
	v_med3_f32 v134, v134, s35, v177
	v_mul_f32_e32 v134, 0xbfb8aa3b, v134
	v_med3_f32 v142, v142, s35, v177
	v_exp_f32_e32 v141, v134
	v_add_f32_e32 v134, 1.0, v147
	v_mul_f32_e32 v142, 0xbfb8aa3b, v142
	v_rcp_f32_e32 v147, v134
	v_max_f32_e32 v134, v148, v148
	v_exp_f32_e32 v148, v142
	v_cvt_pk_f32_fp8_e32 v[144:145], v139
	v_med3_f32 v134, v134, s35, v177
	v_med3_f32 v143, v143, s35, v177
	v_mul_f32_e32 v134, 0xbfb8aa3b, v134
	v_mul_f32_e32 v143, 0xbfb8aa3b, v143
	v_pk_add_f32 v[140:141], v[140:141], 1.0 op_sel_hi:[1,0]
	v_exp_f32_e32 v142, v134
	v_add_f32_e32 v134, 1.0, v148
	v_max_f32_e32 v148, v149, v149
	v_exp_f32_e32 v149, v143
	v_pk_mul_f32 v[140:141], v[146:147], v[140:141]
	v_cvt_pk_f32_fp8_e32 v[150:151], v137
	v_pk_mul_f32 v[6:7], v[6:7], v[140:141]
	v_med3_f32 v140, v144, s35, v177
	v_med3_f32 v148, v148, s35, v177
	v_mul_f32_e32 v140, 0xbfb8aa3b, v140
	v_mul_f32_e32 v143, 0xbfb8aa3b, v148
	v_rcp_f32_e32 v148, v134
	v_add_f32_e32 v134, 1.0, v149
	v_exp_f32_e32 v141, v140
	v_exp_f32_e32 v143, v143
	v_rcp_f32_e32 v149, v134
	v_med3_f32 v134, v150, s35, v177
	v_mul_f32_e32 v134, 0xbfb8aa3b, v134
	v_exp_f32_e32 v140, v134
	v_add_f32_e32 v134, 1.0, v141
	v_pk_add_f32 v[142:143], v[142:143], 1.0 op_sel_hi:[1,0]
	v_med3_f32 v141, v145, s35, v177
	v_pk_mul_f32 v[142:143], v[148:149], v[142:143]
	v_mul_f32_e32 v141, 0xbfb8aa3b, v141
	v_pk_mul_f32 v[8:9], v[8:9], v[142:143]
	v_exp_f32_e32 v143, v141
	v_cvt_pk_f32_fp8_sdwa v[138:139], v139 src0_sel:WORD_1
	v_cvt_pk_f32_fp8_sdwa v[136:137], v137 src0_sel:WORD_1
	v_rcp_f32_e32 v142, v134
	v_med3_f32 v134, v151, s35, v177
	v_mul_f32_e32 v134, 0xbfb8aa3b, v134
	v_exp_f32_e32 v141, v134
	v_add_f32_e32 v134, 1.0, v143
	v_rcp_f32_e32 v143, v134
	v_max_f32_e32 v134, v136, v136
	v_med3_f32 v136, v138, s35, v177
	v_mul_f32_e32 v136, 0xbfb8aa3b, v136
	v_exp_f32_e32 v138, v136
	v_med3_f32 v134, v134, s35, v177
	v_mul_f32_e32 v134, 0xbfb8aa3b, v134
	v_exp_f32_e32 v136, v134
	v_add_f32_e32 v134, 1.0, v138
	v_med3_f32 v138, v139, s35, v177
	v_mul_f32_e32 v138, 0xbfb8aa3b, v138
	v_exp_f32_e32 v139, v138
	v_med3_f32 v137, v137, s35, v177
	v_mul_f32_e32 v137, 0xbfb8aa3b, v137
	v_exp_f32_e32 v137, v137
	v_rcp_f32_e32 v138, v134
	v_add_f32_e32 v134, 1.0, v139
	v_rcp_f32_e32 v139, v134
	v_pk_add_f32 v[136:137], v[136:137], 1.0 op_sel_hi:[1,0]
	v_pk_add_f32 v[140:141], v[140:141], 1.0 op_sel_hi:[1,0]
	v_pk_mul_f32 v[136:137], v[138:139], v[136:137]
	v_pk_mul_f32 v[140:141], v[142:143], v[140:141]
	v_pk_mul_f32 v[4:5], v[4:5], v[136:137]
	v_pk_mul_f32 v[2:3], v[2:3], v[140:141]
	s_nop 0
